# clamp
# speedup vs baseline: 1.1407x; 1.0139x over previous
.LBB0_22:
	s_or_b64 exec, exec, s[10:11]
	v_lshrrev_b32_e32 v45, 5, v0
	v_and_b32_e32 v54, 4, v45
	v_mul_u32_u24_e32 v58, 0xa0, v54
	s_waitcnt lgkmcnt(0)
	s_barrier
	ds_read_b128 v[46:49], v58
	ds_read_b128 v[50:53], v58 offset:16
	v_mov_b32_e32 v3, 0
	v_lshl_add_u64 v[4:5], s[6:7], 0, v[2:3]
	s_mov_b64 s[4:5], 0x16000
	s_waitcnt vmcnt(0) lgkmcnt(1)
	v_fma_f32 v55, v46, v41, v1
	v_fmac_f32_e32 v55, v47, v39
	v_fmac_f32_e32 v55, v48, v37
	v_fmac_f32_e32 v55, v49, v36
	ds_read_b128 v[46:49], v58 offset:32
	s_waitcnt lgkmcnt(1)
	v_fmac_f32_e32 v55, v50, v35
	v_fmac_f32_e32 v55, v51, v34
	v_fmac_f32_e32 v55, v52, v33
	v_fmac_f32_e32 v55, v53, v32
	ds_read_b128 v[50:53], v58 offset:48
	s_waitcnt lgkmcnt(1)
	v_fmac_f32_e32 v55, v46, v42
	v_fmac_f32_e32 v55, v47, v44
	v_fmac_f32_e32 v55, v48, v43
	v_fmac_f32_e32 v55, v49, v40
	ds_read_b128 v[46:49], v58 offset:64
	s_waitcnt lgkmcnt(1)
	v_fmac_f32_e32 v55, v50, v38
	v_fmac_f32_e32 v55, v51, v26
	v_fmac_f32_e32 v55, v52, v27
	v_fmac_f32_e32 v55, v53, v28
	ds_read_b128 v[50:53], v58 offset:80
	s_waitcnt lgkmcnt(1)
	v_fmac_f32_e32 v55, v46, v24
	v_fmac_f32_e32 v55, v47, v29
	v_fmac_f32_e32 v55, v48, v30
	v_fmac_f32_e32 v55, v49, v31
	ds_read_b128 v[46:49], v58 offset:96
	s_waitcnt lgkmcnt(1)
	v_fmac_f32_e32 v55, v50, v25
	v_fmac_f32_e32 v55, v51, v18
	v_fmac_f32_e32 v55, v52, v19
	v_fmac_f32_e32 v55, v53, v20
	ds_read_b128 v[50:53], v58 offset:112
	s_waitcnt lgkmcnt(1)
	v_fmac_f32_e32 v55, v46, v16
	v_fmac_f32_e32 v55, v47, v21
	v_fmac_f32_e32 v55, v48, v22
	v_fmac_f32_e32 v55, v49, v23
	ds_read_b128 v[46:49], v58 offset:128
	s_waitcnt lgkmcnt(1)
	v_fmac_f32_e32 v55, v50, v17
	v_fmac_f32_e32 v55, v51, v10
	v_fmac_f32_e32 v55, v52, v11
	v_fmac_f32_e32 v55, v53, v12
	ds_read_b96 v[50:52], v58 offset:144
	s_waitcnt lgkmcnt(1)
	v_fmac_f32_e32 v55, v46, v7
	v_fmac_f32_e32 v55, v47, v13
	v_fmac_f32_e32 v55, v48, v14
	v_fmac_f32_e32 v55, v49, v15
	ds_read_b128 v[46:49], v58 offset:160
	s_waitcnt lgkmcnt(1)
	v_fmac_f32_e32 v55, v50, v9
	v_add_u32_e32 v2, s3, v54
	v_lshl_add_u64 v[4:5], v[4:5], 0, s[4:5]
	v_fmac_f32_e32 v55, v51, v8
	v_lshlrev_b64 v[50:51], 9, v[2:3]
	v_fmac_f32_e32 v55, v52, v6
	v_lshl_add_u64 v[50:51], v[4:5], 0, v[50:51]
	v_mul_f32_e32 v55, 0xf800000, v55
	global_store_dword v[50:51], v55, off nt
	ds_read_b128 v[50:53], v58 offset:176
	s_waitcnt lgkmcnt(1)
	v_fma_f32 v54, v46, v41, v1
	v_fmac_f32_e32 v54, v47, v39
	v_fmac_f32_e32 v54, v48, v37
	v_fmac_f32_e32 v54, v49, v36
	ds_read_b128 v[46:49], v58 offset:192
	s_waitcnt lgkmcnt(1)
	v_fmac_f32_e32 v54, v50, v35
	v_fmac_f32_e32 v54, v51, v34
	v_fmac_f32_e32 v54, v52, v33
	v_fmac_f32_e32 v54, v53, v32
	ds_read_b128 v[50:53], v58 offset:208
	s_waitcnt lgkmcnt(1)
	v_fmac_f32_e32 v54, v46, v42
	v_fmac_f32_e32 v54, v47, v44
	v_fmac_f32_e32 v54, v48, v43
	v_fmac_f32_e32 v54, v49, v40
	ds_read_b128 v[46:49], v58 offset:224
	s_waitcnt lgkmcnt(1)
	v_fmac_f32_e32 v54, v50, v38
	v_fmac_f32_e32 v54, v51, v26
	v_fmac_f32_e32 v54, v52, v27
	v_fmac_f32_e32 v54, v53, v28
	ds_read_b128 v[50:53], v58 offset:240
	s_waitcnt lgkmcnt(1)
	v_fmac_f32_e32 v54, v46, v24
	v_fmac_f32_e32 v54, v47, v29
	v_fmac_f32_e32 v54, v48, v30
	v_fmac_f32_e32 v54, v49, v31
	ds_read_b128 v[46:49], v58 offset:256
	s_waitcnt lgkmcnt(1)
	v_fmac_f32_e32 v54, v50, v25
	v_fmac_f32_e32 v54, v51, v18
	v_fmac_f32_e32 v54, v52, v19
	v_fmac_f32_e32 v54, v53, v20
	ds_read_b128 v[50:53], v58 offset:272
	s_waitcnt lgkmcnt(1)
	v_fmac_f32_e32 v54, v46, v16
	v_fmac_f32_e32 v54, v47, v21
	v_fmac_f32_e32 v54, v48, v22
	v_fmac_f32_e32 v54, v49, v23
	ds_read_b128 v[46:49], v58 offset:288
	s_waitcnt lgkmcnt(1)
	v_fmac_f32_e32 v54, v50, v17
	v_fmac_f32_e32 v54, v51, v10
	v_fmac_f32_e32 v54, v52, v11
	v_fmac_f32_e32 v54, v53, v12
	ds_read_b96 v[50:52], v58 offset:304
	s_waitcnt lgkmcnt(1)
	v_fmac_f32_e32 v54, v46, v7
	v_fmac_f32_e32 v54, v47, v13
	v_fmac_f32_e32 v54, v48, v14
	v_fmac_f32_e32 v54, v49, v15
	s_waitcnt lgkmcnt(0)
	v_fmac_f32_e32 v54, v50, v9
	ds_read_b128 v[46:49], v58 offset:320
	v_fmac_f32_e32 v54, v51, v8
	v_add_u32_e32 v50, 1, v2
	v_mov_b32_e32 v51, v3
	v_lshlrev_b64 v[50:51], 9, v[50:51]
	v_fmac_f32_e32 v54, v52, v6
	v_lshl_add_u64 v[50:51], v[4:5], 0, v[50:51]
	v_mul_f32_e32 v54, 0xf800000, v54
	global_store_dword v[50:51], v54, off nt
	ds_read_b128 v[50:53], v58 offset:336
	s_waitcnt lgkmcnt(1)
	v_fma_f32 v59, v46, v41, v1
	v_fmac_f32_e32 v59, v47, v39
	v_fmac_f32_e32 v59, v48, v37
	v_fmac_f32_e32 v59, v49, v36
	ds_read_b128 v[46:49], v58 offset:352
	ds_read_b128 v[54:57], v58 offset:368
	s_waitcnt lgkmcnt(2)
	v_fmac_f32_e32 v59, v50, v35
	v_fmac_f32_e32 v59, v51, v34
	v_fmac_f32_e32 v59, v52, v33
	v_fmac_f32_e32 v59, v53, v32
	s_waitcnt lgkmcnt(1)
	v_fmac_f32_e32 v59, v46, v42
	v_fmac_f32_e32 v59, v47, v44
	v_fmac_f32_e32 v59, v48, v43
	v_fmac_f32_e32 v59, v49, v40
	ds_read_b128 v[46:49], v58 offset:384
	ds_read_b128 v[50:53], v58 offset:400
	s_waitcnt lgkmcnt(2)
	v_fmac_f32_e32 v59, v54, v38
	v_fmac_f32_e32 v59, v55, v26
	v_fmac_f32_e32 v59, v56, v27
	v_fmac_f32_e32 v59, v57, v28
	s_waitcnt lgkmcnt(1)
	v_fmac_f32_e32 v59, v46, v24
	v_fmac_f32_e32 v59, v47, v29
	v_fmac_f32_e32 v59, v48, v30
	v_fmac_f32_e32 v59, v49, v31
	ds_read_b128 v[46:49], v58 offset:416
	s_waitcnt lgkmcnt(1)
	v_fmac_f32_e32 v59, v50, v25
	v_fmac_f32_e32 v59, v51, v18
	v_fmac_f32_e32 v59, v52, v19
	v_fmac_f32_e32 v59, v53, v20
	ds_read_b128 v[50:53], v58 offset:432
	s_waitcnt lgkmcnt(1)
	v_fmac_f32_e32 v59, v46, v16
	v_fmac_f32_e32 v59, v47, v21
	v_fmac_f32_e32 v59, v48, v22
	v_fmac_f32_e32 v59, v49, v23
	ds_read_b128 v[46:49], v58 offset:448
	s_waitcnt lgkmcnt(1)
	v_fmac_f32_e32 v59, v50, v17
	v_fmac_f32_e32 v59, v51, v10
	v_fmac_f32_e32 v59, v52, v11
	v_fmac_f32_e32 v59, v53, v12
	ds_read_b96 v[50:52], v58 offset:464
	s_waitcnt lgkmcnt(1)
	v_fmac_f32_e32 v59, v46, v7
	v_fmac_f32_e32 v59, v47, v13
	v_or_b32_e32 v45, 3, v45
	v_fmac_f32_e32 v59, v48, v14
	v_mul_u32_u24_e32 v62, 0xa0, v45
	v_fmac_f32_e32 v59, v49, v15
	ds_read_b128 v[46:49], v62
	s_waitcnt lgkmcnt(1)
	v_fmac_f32_e32 v59, v50, v9
	v_add_u32_e32 v2, 2, v2
	v_fmac_f32_e32 v59, v51, v8
	v_lshlrev_b64 v[50:51], 9, v[2:3]
	v_fmac_f32_e32 v59, v52, v6
	v_lshl_add_u64 v[50:51], v[4:5], 0, v[50:51]
	v_mul_f32_e32 v59, 0xf800000, v59
	global_store_dword v[50:51], v59, off nt
	ds_read_b128 v[50:53], v62 offset:16
	s_waitcnt lgkmcnt(1)
	v_fmac_f32_e32 v1, v46, v41
	v_fmac_f32_e32 v1, v47, v39
	v_fmac_f32_e32 v1, v48, v37
	v_fmac_f32_e32 v1, v49, v36
	ds_read_b128 v[54:57], v62 offset:32
	ds_read_b128 v[58:61], v62 offset:48
	s_waitcnt lgkmcnt(2)
	v_fmac_f32_e32 v1, v50, v35
	v_fmac_f32_e32 v1, v51, v34
	v_fmac_f32_e32 v1, v52, v33
	v_fmac_f32_e32 v1, v53, v32
	s_waitcnt lgkmcnt(1)
	v_fmac_f32_e32 v1, v54, v42
	v_fmac_f32_e32 v1, v55, v44
	v_fmac_f32_e32 v1, v56, v43
	v_fmac_f32_e32 v1, v57, v40
	ds_read_b128 v[32:35], v62 offset:64
	s_waitcnt lgkmcnt(1)
	v_fmac_f32_e32 v1, v58, v38
	v_fmac_f32_e32 v1, v59, v26
	v_fmac_f32_e32 v1, v60, v27
	v_fmac_f32_e32 v1, v61, v28
	ds_read_b128 v[36:39], v62 offset:80
	s_waitcnt lgkmcnt(1)
	v_fmac_f32_e32 v1, v32, v24
	v_fmac_f32_e32 v1, v33, v29
	v_fmac_f32_e32 v1, v34, v30
	v_fmac_f32_e32 v1, v35, v31
	s_waitcnt lgkmcnt(0)
	v_fmac_f32_e32 v1, v36, v25
	ds_read_b128 v[24:27], v62 offset:96
	ds_read_b128 v[28:31], v62 offset:112
	v_fmac_f32_e32 v1, v37, v18
	v_fmac_f32_e32 v1, v38, v19
	v_fmac_f32_e32 v1, v39, v20
	s_waitcnt lgkmcnt(1)
	v_fmac_f32_e32 v1, v24, v16
	v_fmac_f32_e32 v1, v25, v21
	v_fmac_f32_e32 v1, v26, v22
	v_fmac_f32_e32 v1, v27, v23
	s_waitcnt lgkmcnt(0)
	v_fmac_f32_e32 v1, v28, v17
	ds_read_b128 v[16:19], v62 offset:128
	v_fmac_f32_e32 v1, v29, v10
	v_fmac_f32_e32 v1, v30, v11
	v_fmac_f32_e32 v1, v31, v12
	ds_read_b96 v[10:12], v62 offset:144
	s_waitcnt lgkmcnt(1)
	v_fmac_f32_e32 v1, v16, v7
	v_fmac_f32_e32 v1, v17, v13
	v_fmac_f32_e32 v1, v18, v14
	v_fmac_f32_e32 v1, v19, v15
	s_waitcnt lgkmcnt(0)
	v_fmac_f32_e32 v1, v10, v9
	v_add_u32_e32 v2, s3, v45
	v_fmac_f32_e32 v1, v11, v8
	v_lshlrev_b64 v[2:3], 9, v[2:3]
	v_fmac_f32_e32 v1, v12, v6
	v_lshl_add_u64 v[2:3], v[4:5], 0, v[2:3]
	v_mul_f32_e32 v1, 0xf800000, v1
	global_store_dword v[2:3], v1, off nt
	s_mov_b64 s[4:5], 0

.LBB0_44:
	v_lshl_or_b32 v7, s2, 8, v0
	v_and_b32_e32 v2, 31, v0
	v_bfe_u32 v3, v0, 5, 1
	s_cmp_lt_u32 s2, 12
	s_cbranch_scc1 .Lw1f8
	v_lshrrev_b32_e32 v1, 6, v7
	s_cmp_lt_u32 s2, 20
	v_readfirstlane_b32 s10, v1
	s_cbranch_scc1 .Lw2bf
	s_load_dwordx2 s[12:13], s[0:1], 0x20
	s_sub_u32 s10, s10, 0x50
	s_mul_i32 s10, s10, 0xc0
	v_mul_u32_u24_e32 v4, 48, v3
	v_lshl_add_u32 v4, v2, 2, v4
	v_add_u32_e32 v4, s10, v4
	v_add_u32_e32 v5, 0xffffec00, v7
	v_lshlrev_b32_e32 v5, 4, v5
	v_add_u32_e32 v5, 0x14000, v5
	v_mov_b32_e32 v16, 0
	v_mov_b32_e32 v17, 0
	v_mov_b32_e32 v18, 0
	v_mov_b32_e32 v19, 0
	v_mov_b32_e32 v20, 0
	v_mov_b32_e32 v21, 0
	v_mov_b32_e32 v22, 0
	v_mov_b32_e32 v23, 0
	v_cmp_gt_u32_e32 vcc, 3, v2
	s_and_saveexec_b64 s[14:15], vcc
	s_waitcnt lgkmcnt(0)
	global_load_dword v16, v4, s[12:13] offset:0
	global_load_dword v17, v4, s[12:13] offset:12
	global_load_dword v18, v4, s[12:13] offset:24
	global_load_dword v19, v4, s[12:13] offset:36
	global_load_dword v20, v4, s[12:13] offset:96
	global_load_dword v21, v4, s[12:13] offset:108
	global_load_dword v22, v4, s[12:13] offset:120
	global_load_dword v23, v4, s[12:13] offset:132
	s_or_b64 exec, exec, s[14:15]
	s_movk_i32 s16, 0x7fff
	s_mov_b32 s17, 0x7060302
	s_waitcnt vmcnt(7)
	v_mul_f32_e32 v16, 0x6f800000, v16
	v_bfe_u32 v24, v16, 16, 1
	s_waitcnt vmcnt(6)
	v_mul_f32_e32 v17, 0x6f800000, v17
	v_bfe_u32 v25, v17, 16, 1
	s_waitcnt vmcnt(5)
	v_mul_f32_e32 v18, 0x6f800000, v18
	v_bfe_u32 v26, v18, 16, 1
	s_waitcnt vmcnt(4)
	v_mul_f32_e32 v19, 0x6f800000, v19
	v_bfe_u32 v27, v19, 16, 1
	s_waitcnt vmcnt(3)
	v_mul_f32_e32 v20, 0x6f800000, v20
	v_bfe_u32 v28, v20, 16, 1
	s_waitcnt vmcnt(2)
	v_mul_f32_e32 v21, 0x6f800000, v21
	v_bfe_u32 v29, v21, 16, 1
	s_waitcnt vmcnt(1)
	v_mul_f32_e32 v22, 0x6f800000, v22
	v_bfe_u32 v30, v22, 16, 1
	s_waitcnt vmcnt(0)
	v_mul_f32_e32 v23, 0x6f800000, v23
	v_bfe_u32 v31, v23, 16, 1
	v_add3_u32 v16, v16, v24, s16
	v_add3_u32 v17, v17, v25, s16
	v_add3_u32 v18, v18, v26, s16
	v_add3_u32 v19, v19, v27, s16
	v_add3_u32 v20, v20, v28, s16
	v_add3_u32 v21, v21, v29, s16
	v_add3_u32 v22, v22, v30, s16
	v_add3_u32 v23, v23, v31, s16
	v_perm_b32 v0, v17, v16, s17
	v_perm_b32 v1, v19, v18, s17
	v_perm_b32 v2, v21, v20, s17
	v_perm_b32 v3, v23, v22, s17
	global_store_dwordx4 v5, v[0:3], s[6:7]
	s_endpgm

.LBB1_2:
	s_or_b64 exec, exec, s[8:9]
	s_load_dwordx2 s[8:9], s[0:1], 0x20
	s_movk_i32 s3, 0x80
	v_cmp_gt_u32_e32 vcc, s3, v0
	s_and_saveexec_b64 s[10:11], vcc
	s_cbranch_execz .LBB1_4
	s_load_dwordx2 s[0:1], s[0:1], 0x10
	v_lshlrev_b32_e32 v3, 2, v0
	s_waitcnt lgkmcnt(0)
	global_load_dword v4, v3, s[0:1]
	v_add_u32_e32 v3, 0, v3
	v_add_u32_e32 v3, 0x18000, v3
	s_waitcnt vmcnt(0)
	v_mul_f32_e32 v4, 0xf800000, v4
	ds_write_b32 v3, v4
.LBB1_4:
	s_or_b64 exec, exec, s[10:11]
	v_lshl_or_b32 v221, s2, 4, v1
	v_lshlrev_b32_e32 v10, 7, v221
	v_and_or_b32 v0, v0, 31, v10
	v_lshrrev_b32_e32 v3, 5, v220
	v_mul_lo_u32 v160, v0, 27
	v_mov_b32_e32 v161, 0
	s_add_u32 s0, s6, 0x16000
	v_mul_u32_u24_e32 v3, 14, v3
	v_lshl_add_u64 v[0:1], v[160:161], 2, s[4:5]
	v_add_u32_e32 v160, 0x360, v160
	s_addc_u32 s1, s7, 0
	v_lshlrev_b32_e32 v4, 2, v3
	v_mov_b32_e32 v5, v161
	v_lshl_add_u64 v[8:9], v[160:161], 2, s[4:5]
	v_lshl_or_b32 v160, v220, 1, v10
	v_lshl_add_u64 v[6:7], v[0:1], 0, v[4:5]
	v_lshl_add_u64 v[10:11], v[160:161], 2, s[0:1]
	v_or_b32_e32 v160, 0x400, v160
	global_load_dwordx4 v[182:185], v[6:7], off
	global_load_dwordx4 v[178:181], v[6:7], off offset:32
	global_load_dwordx4 v[198:201], v[6:7], off offset:16
	v_lshl_add_u64 v[12:13], v[160:161], 2, s[0:1]
	global_load_dwordx2 v[14:15], v[10:11], off
	global_load_dwordx2 v[16:17], v[12:13], off
	global_load_dword v222, v[0:1], off offset:52
	v_lshl_add_u64 v[0:1], v[8:9], 0, v[4:5]
	global_load_dword v223, v[0:1], off offset:48
	global_load_dwordx4 v[186:189], v[0:1], off offset:32
	global_load_dwordx4 v[194:197], v[0:1], off offset:16
	global_load_dword v225, v[6:7], off offset:48
	global_load_dwordx4 v[190:193], v[0:1], off
	global_load_dword v224, v[8:9], off offset:52
	s_add_u32 s6, s6, 0x216000
	s_load_dwordx2 s[10:11], s[12:13], 0x0
	s_load_dword s18, s[12:13], 0x8
	s_addc_u32 s7, s7, 0
	s_add_i32 s12, 0, 0x16000
	v_add_u32_e32 v228, s12, v2
	v_lshl_add_u32 v1, v220, 3, v228
	v_mov_b32_e32 v160, v161
	s_mov_b32 s16, 0
	v_cmp_gt_u32_e64 s[0:1], 32, v220
	v_cmp_eq_u32_e64 s[2:3], 0, v220
	v_mov_b32_e32 v226, 0x7f
	v_mov_b32_e32 v227, 27
	v_mov_b32_e32 v230, 0
	v_mov_b64_e32 v[218:219], v[160:161]
	s_waitcnt vmcnt(0)
	v_mov_b32_e32 v0, v183
	v_mov_b32_e32 v25, v184
	v_mov_b32_e32 v162, v199
	ds_write2st64_b64 v1, v[14:15], v[16:17] offset1:1
	s_waitcnt vmcnt(0)
	v_mbcnt_lo_u32_b32 v1, -1, 0
	v_mov_b32_e32 v163, v200
	v_mov_b32_e32 v200, v179
	v_mov_b32_e32 v179, v180
	v_mbcnt_hi_u32_b32 v229, -1, v1
	s_waitcnt lgkmcnt(0)
	s_barrier
	s_branch .LBB1_7

.LBB1_12:
	s_and_b32 s12, s19, 1
	s_lshr_b32 s13, s19, 1
	s_add_i32 s16, s19, 1
	v_lshl_add_u32 v231, s13, 3, v221
	s_cmp_lg_u32 s19, 3
	s_cselect_b32 s17, s16, 3
	s_waitcnt lgkmcnt(2)
	v_lshlrev_b32_e32 v2, 7, v231
	s_lshl_b32 s14, s12, 6
	v_or3_b32 v160, v2, s14, v220
	s_waitcnt lgkmcnt(0)
	v_mov_b32_e32 v1, v220
	v_lshl_add_u64 v[2:3], v[160:161], 2, s[6:7]
	global_load_dword v232, v[2:3], off
	s_lshl_b32 s14, s17, 2
	s_and_b32 s14, s14, 24
	s_lshl_b32 s13, s13, 9
	v_lshrrev_b32_e32 v3, 5, v1
	s_cmp_eq_u32 s12, 0
	v_add_u32_e32 v2, s14, v221
	v_lshlrev_b32_e32 v206, 4, v3
	s_cselect_b64 s[14:15], -1, 0
	s_cmp_eq_u32 s12, 1
	v_add3_u32 v149, v228, s13, v206
	s_cselect_b64 s[12:13], -1, 0
	s_lshl_b32 s17, s17, 6
	s_and_b32 s17, s17, 64
	v_lshl_or_b32 v2, v2, 7, s17
	v_lshl_add_u32 v234, v1, 4, 0
	v_and_or_b32 v1, v1, 31, v2
	v_mul_lo_u32 v2, v1, 27
	v_add_u32_e32 v233, 0xc000, v234
	v_mad_u64_u32 v[204:205], s[20:21], v3, 14, v[2:3]
	v_add_u32_e32 v202, 13, v2
	s_waitcnt vmcnt(3)
	v_mul_f32_e32 v1, 0.15915494, v222
	v_cos_f32_e32 v2, v1
	v_sin_f32_e32 v1, v1
	v_add_f32_e32 v2, v2, v2
	v_cndmask_b32_e64 v3, v2, v1, s[0:1]
	v_mul_f32_e32 v1, v1, v2
	v_fma_f32 v2, v2, v2, -2.0
	v_cndmask_b32_e64 v4, v2, v1, s[0:1]
	v_mul_f32_e32 v207, v1, v2
	v_fma_f32 v208, v2, v2, -2.0
	v_mul_f32_e32 v2, 0.15915494, v182
	v_cvt_pk_fp8_f32 v131, v225, v3
	v_cos_f32_e32 v3, v2
	v_sin_f32_e32 v2, v2
	v_cndmask_b32_e64 v1, v208, v207, s[0:1]
	v_cvt_pk_fp8_f32 v131, v4, v1 op_sel:[0,0,1]
	v_add_f32_e32 v1, v3, v3
	v_cvt_pk_f16_f32 v1, v2, v1
	v_cvt_pk_fp8_f32 v128, v182, v0
	v_cvt_scalef32_pk_fp8_f16 v132, v1, 1.0
	v_pk_fma_f16 v1, v1, v1, -2.0 op_sel:[1,0,1] op_sel_hi:[1,1,0]
	v_mul_f32_e32 v0, 0.15915494, v0
	v_cvt_scalef32_pk_fp8_f16 v132, v1, 1.0 op_sel:[0,0,1]
	v_pk_fma_f16 v1, v1, v1, -2.0 op_sel:[0,1,1] op_sel_hi:[1,1,0]
	v_cos_f32_e32 v2, v0
	v_cvt_scalef32_pk_fp8_f16 v133, v1, 1.0
	v_pk_fma_f16 v1, v1, v1, -2.0 op_sel:[0,1,1] op_sel_hi:[1,1,0]
	v_sin_f32_e32 v0, v0
	v_cvt_scalef32_pk_fp8_f16 v133, v1, 1.0 op_sel:[0,0,1]
	v_pk_fma_f16 v1, v1, v1, -2.0 op_sel:[0,1,1] op_sel_hi:[1,1,0]
	s_nop 0
	v_cvt_scalef32_pk_fp8_f16 v134, v1, 1.0
	v_pk_fma_f16 v1, v1, v1, -2.0 op_sel:[0,1,1] op_sel_hi:[1,1,0]
	s_nop 0
	v_cvt_scalef32_pk_fp8_f16 v134, v1, 1.0 op_sel:[0,0,1]
	v_add_f32_e32 v1, v2, v2
	v_cvt_pk_f16_f32 v0, v0, v1
	v_cvt_scalef32_pk_fp8_f16 v135, v0, 1.0
	v_pk_fma_f16 v24, v0, v0, -2.0 op_sel:[1,0,1] op_sel_hi:[1,1,0]
	s_waitcnt vmcnt(2)
	v_mul_f32_e32 v0, 0.15915494, v224
	v_cos_f32_e32 v1, v0
	v_sin_f32_e32 v0, v0
	v_add_f32_e32 v1, v1, v1
	v_cndmask_b32_e64 v2, v1, v0, s[0:1]
	v_mul_f32_e32 v0, v0, v1
	v_fma_f32 v1, v1, v1, -2.0
	v_cndmask_b32_e64 v3, v1, v0, s[0:1]
	v_mul_f32_e32 v209, v0, v1
	v_fma_f32 v210, v1, v1, -2.0
	v_mul_f32_e32 v1, 0.15915494, v190
	s_waitcnt vmcnt(1)
	v_cvt_pk_fp8_f32 v19, v223, v2
	v_cos_f32_e32 v2, v1
	v_sin_f32_e32 v1, v1
	v_cndmask_b32_e64 v0, v210, v209, s[0:1]
	v_cvt_pk_fp8_f32 v19, v3, v0 op_sel:[0,0,1]
	v_add_f32_e32 v0, v2, v2
	v_cvt_pk_f16_f32 v0, v1, v0
	v_cvt_scalef32_pk_fp8_f16 v20, v0, 1.0
	v_pk_fma_f16 v0, v0, v0, -2.0 op_sel:[1,0,1] op_sel_hi:[1,1,0]
	v_mul_f32_e32 v1, 0.15915494, v191
	v_cvt_scalef32_pk_fp8_f16 v135, v24, 1.0 op_sel:[0,0,1]
	v_cvt_scalef32_pk_fp8_f16 v20, v0, 1.0 op_sel:[0,0,1]
	v_pk_fma_f16 v0, v0, v0, -2.0 op_sel:[0,1,1] op_sel_hi:[1,1,0]
	v_cos_f32_e32 v2, v1
	v_pk_fma_f16 v24, v24, v24, -2.0 op_sel:[0,1,1] op_sel_hi:[1,1,0]
	v_cvt_scalef32_pk_fp8_f16 v21, v0, 1.0
	v_pk_fma_f16 v0, v0, v0, -2.0 op_sel:[0,1,1] op_sel_hi:[1,1,0]
	v_sin_f32_e32 v1, v1
	v_pk_fma_f16 v35, v24, v24, -2.0 op_sel:[0,1,1] op_sel_hi:[1,1,0]
	v_cvt_pk_fp8_f32 v128, v25, v185 op_sel:[0,0,1]
	v_cvt_scalef32_pk_fp8_f16 v21, v0, 1.0 op_sel:[0,0,1]
	v_pk_fma_f16 v0, v0, v0, -2.0 op_sel:[0,1,1] op_sel_hi:[1,1,0]
	v_pk_fma_f16 v36, v35, v35, -2.0 op_sel:[0,1,1] op_sel_hi:[1,1,0]
	v_mul_f32_e32 v25, 0.15915494, v25
	v_cvt_pk_fp8_f32 v129, v198, v162
	v_cvt_pk_fp8_f32 v130, v178, v200
	v_cvt_pk_fp8_f32 v16, v190, v191
	v_cvt_pk_fp8_f32 v17, v194, v195
	v_cvt_pk_fp8_f32 v18, v186, v187
	v_cvt_scalef32_pk_fp8_f16 v22, v0, 1.0
	v_pk_fma_f16 v0, v0, v0, -2.0 op_sel:[0,1,1] op_sel_hi:[1,1,0]
	v_pk_fma_f16 v37, v36, v36, -2.0 op_sel:[0,1,1] op_sel_hi:[1,1,0]
	v_cvt_scalef32_pk_fp8_f16 v137, v36, 1.0
	v_cos_f32_e32 v36, v25
	v_cvt_scalef32_pk_fp8_f16 v22, v0, 1.0 op_sel:[0,0,1]
	v_add_f32_e32 v0, v2, v2
	v_sin_f32_e32 v25, v25
	v_cvt_pk_f16_f32 v0, v1, v0
	v_mov_b32_e32 v160, v204
	v_cvt_scalef32_pk_fp8_f16 v23, v0, 1.0
	v_pk_fma_f16 v34, v0, v0, -2.0 op_sel:[1,0,1] op_sel_hi:[1,1,0]
	ds_read_b128 v[26:29], v234
	ds_read_b128 v[30:33], v234 offset:1024
	ds_read_b128 v[8:11], v234 offset:2048
	ds_read_b128 v[12:15], v234 offset:3072
	ds_read_b128 v[0:3], v234 offset:4096
	ds_read_b128 v[4:7], v234 offset:5120
	ds_read_b128 v[152:155], v234 offset:6144
	ds_read_b128 v[156:159], v234 offset:7168
	ds_read_b128 v[96:99], v149
	ds_read_b128 v[100:103], v149 offset:32
	ds_read_b128 v[104:107], v149 offset:64
	ds_read_b128 v[108:111], v149 offset:96
	v_cvt_pk_fp8_f32 v129, v163, v201 op_sel:[0,0,1]
	v_cvt_pk_fp8_f32 v130, v179, v181 op_sel:[0,0,1]
	v_cvt_pk_fp8_f32 v16, v192, v193 op_sel:[0,0,1]
	v_cvt_pk_fp8_f32 v17, v196, v197 op_sel:[0,0,1]
	v_cvt_pk_fp8_f32 v18, v188, v189 op_sel:[0,0,1]
	v_cvt_scalef32_pk_fp8_f16 v136, v24, 1.0
	v_add_f32_e32 v24, v36, v36
	v_cvt_pk_f16_f32 v24, v25, v24
	v_pk_fma_f16 v25, v24, v24, -2.0 op_sel:[1,0,1] op_sel_hi:[1,1,0]
	v_cvt_scalef32_pk_fp8_f16 v138, v24, 1.0
	v_cvt_scalef32_pk_fp8_f16 v23, v34, 1.0 op_sel:[0,0,1]
	v_cvt_scalef32_pk_fp8_f16 v136, v35, 1.0 op_sel:[0,0,1]
	v_pk_fma_f16 v35, v25, v25, -2.0 op_sel:[0,1,1] op_sel_hi:[1,1,0]
	v_cvt_scalef32_pk_fp8_f16 v138, v25, 1.0 op_sel:[0,0,1]
	v_mul_f32_e32 v25, 0.15915494, v185
	s_waitcnt lgkmcnt(0)
	v_mfma_scale_f32_32x32x64_f8f6f4 v[112:127], v[26:33], v[16:23], v[96:111], v227, v226 op_sel_hi:[0,0,0]
	v_cvt_scalef32_pk_fp8_f16 v139, v35, 1.0
	v_pk_fma_f16 v35, v35, v35, -2.0 op_sel:[0,1,1] op_sel_hi:[1,1,0]
	s_nop 0
	v_pk_fma_f16 v24, v35, v35, -2.0 op_sel:[0,1,1] op_sel_hi:[1,1,0]
	ds_read_b128 v[64:67], v149 offset:128
	ds_read_b128 v[68:71], v149 offset:160
	ds_read_b128 v[72:75], v149 offset:192
	ds_read_b128 v[76:79], v149 offset:224
	v_cvt_scalef32_pk_fp8_f16 v140, v24, 1.0
	v_pk_fma_f16 v24, v24, v24, -2.0 op_sel:[0,1,1] op_sel_hi:[1,1,0]
	v_cvt_scalef32_pk_fp8_f16 v137, v37, 1.0 op_sel:[0,0,1]
	v_cvt_scalef32_pk_fp8_f16 v140, v24, 1.0 op_sel:[0,0,1]
	v_cvt_scalef32_pk_fp8_f16 v139, v35, 1.0 op_sel:[0,0,1]
	v_mfma_scale_f32_32x32x64_f8f6f4 v[96:111], v[26:33], v[128:135], v[96:111], v227, v226 op_sel_hi:[0,0,0]
	v_cos_f32_e32 v26, v25
	v_sin_f32_e32 v25, v25
	v_mul_f32_e32 v30, 0.15915494, v192
	v_mul_f32_e32 v31, 0.15915494, v193
	v_add_f32_e32 v24, v26, v26
	v_cvt_pk_f16_f32 v24, v25, v24
	v_cvt_scalef32_pk_fp8_f16 v141, v24, 1.0
	v_pk_fma_f16 v24, v24, v24, -2.0 op_sel:[1,0,1] op_sel_hi:[1,1,0]
	s_nop 0
	v_cvt_scalef32_pk_fp8_f16 v141, v24, 1.0 op_sel:[0,0,1]
	v_pk_fma_f16 v26, v24, v24, -2.0 op_sel:[0,1,1] op_sel_hi:[1,1,0]
	v_lshl_add_u64 v[24:25], v[160:161], 2, s[4:5]
	v_pk_fma_f16 v27, v26, v26, -2.0 op_sel:[0,1,1] op_sel_hi:[1,1,0]
	s_nop 0
	v_pk_fma_f16 v28, v27, v27, -2.0 op_sel:[0,1,1] op_sel_hi:[1,1,0]
	s_waitcnt lgkmcnt(0)
	v_mfma_scale_f32_32x32x64_f8f6f4 v[80:95], v[8:15], v[16:23], v[64:79], v227, v226 op_sel_hi:[0,0,0]
	global_load_dwordx4 v[182:185], v[24:25], off
	global_load_dwordx4 v[190:193], v[24:25], off offset:3456
	v_cos_f32_e32 v25, v31
	v_pk_fma_f16 v29, v28, v28, -2.0 op_sel:[0,1,1] op_sel_hi:[1,1,0]
	v_cvt_scalef32_pk_fp8_f16 v143, v28, 1.0
	v_cvt_scalef32_pk_fp8_f16 v142, v26, 1.0
	v_cvt_scalef32_pk_fp8_f16 v143, v29, 1.0 op_sel:[0,0,1]
	v_cvt_scalef32_pk_fp8_f16 v142, v27, 1.0 op_sel:[0,0,1]
	v_add_f32_e32 v150, v25, v25
	v_mfma_scale_f32_32x32x64_f8f6f4 v[64:79], v[8:15], v[128:135], v[64:79], v227, v226 op_sel_hi:[0,0,0]
	v_pk_fma_f16 v8, v34, v34, -2.0 op_sel:[0,1,1] op_sel_hi:[1,1,0]
	ds_read_b128 v[32:35], v149 offset:256
	ds_read_b128 v[36:39], v149 offset:288
	ds_read_b128 v[40:43], v149 offset:320
	ds_read_b128 v[44:47], v149 offset:352
	v_pk_fma_f16 v9, v8, v8, -2.0 op_sel:[0,1,1] op_sel_hi:[1,1,0]
	v_cvt_scalef32_pk_fp8_f16 v144, v8, 1.0
	v_pk_fma_f16 v10, v9, v9, -2.0 op_sel:[0,1,1] op_sel_hi:[1,1,0]
	v_cvt_scalef32_pk_fp8_f16 v144, v9, 1.0 op_sel:[0,0,1]
	v_pk_fma_f16 v11, v10, v10, -2.0 op_sel:[0,1,1] op_sel_hi:[1,1,0]
	v_cvt_scalef32_pk_fp8_f16 v145, v10, 1.0
	v_cos_f32_e32 v10, v30
	v_cvt_scalef32_pk_fp8_f16 v145, v11, 1.0 op_sel:[0,0,1]
	v_sin_f32_e32 v11, v30
	v_add_f32_e32 v8, v10, v10
	v_cvt_pk_f16_f32 v8, v11, v8
	v_pk_fma_f16 v9, v8, v8, -2.0 op_sel:[1,0,1] op_sel_hi:[1,1,0]
	v_cvt_scalef32_pk_fp8_f16 v146, v8, 1.0
	v_pk_fma_f16 v10, v9, v9, -2.0 op_sel:[0,1,1] op_sel_hi:[1,1,0]
	s_waitcnt lgkmcnt(0)
	v_mfma_scale_f32_32x32x64_f8f6f4 v[48:63], v[0:7], v[16:23], v[32:47], v227, v226 op_sel_hi:[0,0,0]
	v_cvt_scalef32_pk_fp8_f16 v147, v10, 1.0
	v_pk_fma_f16 v10, v10, v10, -2.0 op_sel:[0,1,1] op_sel_hi:[1,1,0]
	v_cvt_scalef32_pk_fp8_f16 v146, v9, 1.0 op_sel:[0,0,1]
	v_cvt_scalef32_pk_fp8_f16 v147, v10, 1.0 op_sel:[0,0,1]
	v_pk_fma_f16 v24, v10, v10, -2.0 op_sel:[0,1,1] op_sel_hi:[1,1,0]
	s_nop 0
	v_cvt_scalef32_pk_fp8_f16 v148, v24, 1.0
	v_pk_fma_f16 v24, v24, v24, -2.0 op_sel:[0,1,1] op_sel_hi:[1,1,0]
	s_nop 0
	v_cvt_scalef32_pk_fp8_f16 v148, v24, 1.0 op_sel:[0,0,1]
	v_mfma_scale_f32_32x32x64_f8f6f4 v[32:47], v[0:7], v[128:135], v[32:47], v227, v226 op_sel_hi:[0,0,0]
	ds_read_b128 v[0:3], v149 offset:384
	ds_read_b128 v[4:7], v149 offset:416
	ds_read_b128 v[8:11], v149 offset:448
	ds_read_b128 v[12:15], v149 offset:480
	v_sin_f32_e32 v149, v31
	s_nop 0
	v_cvt_pk_f16_f32 v150, v149, v150
	v_cvt_scalef32_pk_fp8_f16 v149, v150, 1.0
	v_pk_fma_f16 v150, v150, v150, -2.0 op_sel:[1,0,1] op_sel_hi:[1,1,0]
	s_nop 0
	v_pk_fma_f16 v160, v150, v150, -2.0 op_sel:[0,1,1] op_sel_hi:[1,1,0]
	v_cvt_scalef32_pk_fp8_f16 v149, v150, 1.0 op_sel:[0,0,1]
	v_pk_fma_f16 v164, v160, v160, -2.0 op_sel:[0,1,1] op_sel_hi:[1,1,0]
	s_nop 0
	v_pk_fma_f16 v150, v164, v164, -2.0 op_sel:[0,1,1] op_sel_hi:[1,1,0]
	s_waitcnt lgkmcnt(0)
	v_mfma_scale_f32_32x32x64_f8f6f4 v[16:31], v[152:159], v[16:23], v[0:15], v227, v226 op_sel_hi:[0,0,0]
	v_pk_fma_f16 v165, v150, v150, -2.0 op_sel:[0,1,1] op_sel_hi:[1,1,0]
	v_cvt_scalef32_pk_fp8_f16 v151, v150, 1.0
	v_cvt_scalef32_pk_fp8_f16 v150, v160, 1.0
	v_cvt_scalef32_pk_fp8_f16 v151, v165, 1.0 op_sel:[0,0,1]
	v_cvt_scalef32_pk_fp8_f16 v150, v164, 1.0 op_sel:[0,0,1]
	v_mfma_scale_f32_32x32x64_f8f6f4 v[0:15], v[152:159], v[128:135], v[0:15], v227, v226 op_sel_hi:[0,0,0]
	v_mul_f32_e32 v128, 0.15915494, v198
	v_cos_f32_e32 v129, v128
	v_sin_f32_e32 v128, v128
	v_mul_f32_e32 v133, 0.15915494, v162
	v_cos_f32_e32 v134, v133
	v_add_f32_e32 v129, v129, v129
	v_cvt_pk_f16_f32 v130, v128, v129
	v_pk_fma_f16 v131, v130, v130, -2.0 op_sel:[1,0,1] op_sel_hi:[1,1,0]
	v_sin_f32_e32 v133, v133
	v_pk_fma_f16 v128, v131, v131, -2.0 op_sel:[0,1,1] op_sel_hi:[1,1,0]
	s_nop 0
	v_pk_fma_f16 v132, v128, v128, -2.0 op_sel:[0,1,1] op_sel_hi:[1,1,0]
	v_cvt_scalef32_pk_fp8_f16 v129, v128, 1.0
	v_cvt_scalef32_pk_fp8_f16 v128, v130, 1.0
	v_add_f32_e32 v130, v134, v134
	v_cvt_scalef32_pk_fp8_f16 v128, v131, 1.0 op_sel:[0,0,1]
	v_cvt_pk_f16_f32 v130, v133, v130
	v_cvt_scalef32_pk_fp8_f16 v129, v132, 1.0 op_sel:[0,0,1]
	v_cvt_scalef32_pk_fp8_f16 v131, v130, 1.0
	v_pk_fma_f16 v133, v130, v130, -2.0 op_sel:[1,0,1] op_sel_hi:[1,1,0]
	v_pk_fma_f16 v132, v132, v132, -2.0 op_sel:[0,1,1] op_sel_hi:[1,1,0]
	ds_read_b128 v[152:155], v234 offset:8192
	ds_read_b128 v[156:159], v234 offset:9216
	ds_read_b128 v[164:167], v234 offset:10240
	ds_read_b128 v[168:171], v234 offset:11264
	ds_read_b128 v[236:239], v234 offset:12288
	ds_read_b128 v[240:243], v234 offset:13312
	v_cvt_scalef32_pk_fp8_f16 v130, v132, 1.0
	v_pk_fma_f16 v132, v132, v132, -2.0 op_sel:[0,1,1] op_sel_hi:[1,1,0]
	v_mul_f32_e32 v135, 0.15915494, v163
	s_waitcnt lgkmcnt(4)
	v_mfma_scale_f32_32x32x64_f8f6f4 v[96:111], v[152:159], v[136:143], v[96:111], v227, v226 op_sel_hi:[0,0,0]
	v_cvt_scalef32_pk_fp8_f16 v131, v133, 1.0 op_sel:[0,0,1]
	v_pk_fma_f16 v133, v133, v133, -2.0 op_sel:[0,1,1] op_sel_hi:[1,1,0]
	v_cvt_scalef32_pk_fp8_f16 v130, v132, 1.0 op_sel:[0,0,1]
	v_cvt_scalef32_pk_fp8_f16 v132, v133, 1.0
	v_pk_fma_f16 v133, v133, v133, -2.0 op_sel:[0,1,1] op_sel_hi:[1,1,0]
	ds_read_b128 v[244:247], v234 offset:14336
	ds_read_b128 v[248:251], v234 offset:15360
	v_pk_fma_f16 v134, v133, v133, -2.0 op_sel:[0,1,1] op_sel_hi:[1,1,0]
	v_cvt_scalef32_pk_fp8_f16 v132, v133, 1.0 op_sel:[0,0,1]
	v_cvt_scalef32_pk_fp8_f16 v133, v134, 1.0
	v_pk_fma_f16 v134, v134, v134, -2.0 op_sel:[0,1,1] op_sel_hi:[1,1,0]
	s_nop 0
	v_cvt_scalef32_pk_fp8_f16 v133, v134, 1.0 op_sel:[0,0,1]
	v_mfma_scale_f32_32x32x64_f8f6f4 v[112:127], v[152:159], v[144:151], v[112:127], v227, v226 op_sel_hi:[0,0,0]
	v_cos_f32_e32 v152, v135
	v_sin_f32_e32 v135, v135
	v_mul_f32_e32 v154, 0.15915494, v194
	v_cos_f32_e32 v155, v154
	v_add_f32_e32 v134, v152, v152
	v_cvt_pk_f16_f32 v152, v135, v134
	v_pk_fma_f16 v153, v152, v152, -2.0 op_sel:[1,0,1] op_sel_hi:[1,1,0]
	v_sin_f32_e32 v154, v154
	v_pk_fma_f16 v134, v153, v153, -2.0 op_sel:[0,1,1] op_sel_hi:[1,1,0]
	s_nop 0
	v_pk_fma_f16 v160, v134, v134, -2.0 op_sel:[0,1,1] op_sel_hi:[1,1,0]
	v_cvt_scalef32_pk_fp8_f16 v135, v134, 1.0
	v_cvt_scalef32_pk_fp8_f16 v134, v152, 1.0
	v_add_f32_e32 v152, v155, v155
	s_waitcnt lgkmcnt(4)
	v_mfma_scale_f32_32x32x64_f8f6f4 v[64:79], v[164:171], v[136:143], v[64:79], v227, v226 op_sel_hi:[0,0,0]
	v_mul_f32_e32 v157, 0.15915494, v195
	v_cvt_pk_f16_f32 v154, v154, v152
	v_cos_f32_e32 v158, v157
	v_pk_fma_f16 v155, v154, v154, -2.0 op_sel:[1,0,1] op_sel_hi:[1,1,0]
	v_sin_f32_e32 v157, v157
	v_pk_fma_f16 v152, v155, v155, -2.0 op_sel:[0,1,1] op_sel_hi:[1,1,0]
	v_cvt_scalef32_pk_fp8_f16 v134, v153, 1.0 op_sel:[0,0,1]
	v_pk_fma_f16 v156, v152, v152, -2.0 op_sel:[0,1,1] op_sel_hi:[1,1,0]
	v_cvt_scalef32_pk_fp8_f16 v153, v152, 1.0
	v_cvt_scalef32_pk_fp8_f16 v152, v154, 1.0
	v_add_f32_e32 v154, v158, v158
	v_mul_f32_e32 v159, 0.15915494, v196
	v_cvt_scalef32_pk_fp8_f16 v152, v155, 1.0 op_sel:[0,0,1]
	v_mfma_scale_f32_32x32x64_f8f6f4 v[80:95], v[164:171], v[144:151], v[80:95], v227, v226 op_sel_hi:[0,0,0]
	v_cvt_pk_f16_f32 v154, v157, v154
	v_cvt_scalef32_pk_fp8_f16 v153, v156, 1.0 op_sel:[0,0,1]
	v_cvt_scalef32_pk_fp8_f16 v155, v154, 1.0
	v_pk_fma_f16 v156, v156, v156, -2.0 op_sel:[0,1,1] op_sel_hi:[1,1,0]
	v_pk_fma_f16 v157, v154, v154, -2.0 op_sel:[1,0,1] op_sel_hi:[1,1,0]
	v_cvt_scalef32_pk_fp8_f16 v154, v156, 1.0
	v_pk_fma_f16 v156, v156, v156, -2.0 op_sel:[0,1,1] op_sel_hi:[1,1,0]
	v_cvt_scalef32_pk_fp8_f16 v155, v157, 1.0 op_sel:[0,0,1]
	v_pk_fma_f16 v157, v157, v157, -2.0 op_sel:[0,1,1] op_sel_hi:[1,1,0]
	v_cvt_scalef32_pk_fp8_f16 v154, v156, 1.0 op_sel:[0,0,1]
	v_cvt_scalef32_pk_fp8_f16 v156, v157, 1.0
	v_pk_fma_f16 v157, v157, v157, -2.0 op_sel:[0,1,1] op_sel_hi:[1,1,0]
	s_waitcnt lgkmcnt(0)
	v_mfma_scale_f32_32x32x64_f8f6f4 v[0:15], v[244:251], v[136:143], v[0:15], v227, v226 op_sel_hi:[0,0,0]
	v_cvt_scalef32_pk_fp8_f16 v156, v157, 1.0 op_sel:[0,0,1]
	v_pk_fma_f16 v158, v157, v157, -2.0 op_sel:[0,1,1] op_sel_hi:[1,1,0]
	v_cvt_scalef32_pk_fp8_f16 v135, v160, 1.0 op_sel:[0,0,1]
	v_cvt_scalef32_pk_fp8_f16 v157, v158, 1.0
	v_mfma_scale_f32_32x32x64_f8f6f4 v[32:47], v[236:243], v[136:143], v[32:47], v227, v226 op_sel_hi:[0,0,0]
	v_cos_f32_e32 v136, v159
	v_sin_f32_e32 v137, v159
	v_pk_fma_f16 v138, v158, v158, -2.0 op_sel:[0,1,1] op_sel_hi:[1,1,0]
	v_add_f32_e32 v136, v136, v136
	v_cvt_pk_f16_f32 v136, v137, v136
	v_pk_fma_f16 v137, v136, v136, -2.0 op_sel:[1,0,1] op_sel_hi:[1,1,0]
	v_cvt_scalef32_pk_fp8_f16 v157, v138, 1.0 op_sel:[0,0,1]
	v_pk_fma_f16 v138, v137, v137, -2.0 op_sel:[0,1,1] op_sel_hi:[1,1,0]
	s_nop 0
	v_pk_fma_f16 v180, v138, v138, -2.0 op_sel:[0,1,1] op_sel_hi:[1,1,0]
	v_cvt_scalef32_pk_fp8_f16 v159, v138, 1.0
	v_cvt_scalef32_pk_fp8_f16 v158, v136, 1.0
	v_cvt_scalef32_pk_fp8_f16 v159, v180, 1.0 op_sel:[0,0,1]
	v_cvt_scalef32_pk_fp8_f16 v158, v137, 1.0 op_sel:[0,0,1]
	v_mfma_scale_f32_32x32x64_f8f6f4 v[48:63], v[236:243], v[144:151], v[48:63], v227, v226 op_sel_hi:[0,0,0]
	v_mfma_scale_f32_32x32x64_f8f6f4 v[16:31], v[244:251], v[144:151], v[16:31], v227, v226 op_sel_hi:[0,0,0]
	ds_read_b128 v[140:143], v234 offset:16384
	ds_read_b128 v[144:147], v234 offset:17408
	ds_read_b128 v[236:239], v234 offset:18432
	ds_read_b128 v[240:243], v234 offset:19456
	ds_read_b128 v[170:173], v234 offset:20480
	ds_read_b128 v[174:177], v234 offset:21504
	s_waitcnt lgkmcnt(4)
	v_mfma_scale_f32_32x32x64_f8f6f4 v[96:111], v[140:147], v[128:135], v[96:111], v227, v226 op_sel_hi:[0,0,0]
	v_pk_fma_f16 v139, v160, v160, -2.0 op_sel:[0,1,1] op_sel_hi:[1,1,0]
	v_mov_b32_e32 v160, v204
	ds_read_b128 v[162:165], v234 offset:22528
	ds_read_b128 v[166:169], v234 offset:23552
	v_mul_f32_e32 v136, 0.15915494, v201
	v_cos_f32_e32 v137, v136
	v_sin_f32_e32 v136, v136
	v_mul_f32_e32 v150, 0.15915494, v186
	v_cos_f32_e32 v151, v150
	v_add_f32_e32 v137, v137, v137
	v_cvt_pk_f16_f32 v136, v136, v137
	v_pk_fma_f16 v138, v136, v136, -2.0 op_sel:[1,0,1] op_sel_hi:[1,1,0]
	v_cvt_scalef32_pk_fp8_f16 v137, v136, 1.0
	v_mfma_scale_f32_32x32x64_f8f6f4 v[112:127], v[140:147], v[152:159], v[112:127], v227, v226 op_sel_hi:[0,0,0]
	v_mul_f32_e32 v140, 0.15915494, v178
	v_cos_f32_e32 v141, v140
	v_sin_f32_e32 v140, v140
	v_mul_f32_e32 v143, 0.15915494, v200
	v_cos_f32_e32 v144, v143
	v_add_f32_e32 v141, v141, v141
	v_cvt_pk_f16_f32 v141, v140, v141
	v_sin_f32_e32 v143, v143
	v_cvt_scalef32_pk_fp8_f16 v140, v141, 1.0
	v_pk_fma_f16 v141, v141, v141, -2.0 op_sel:[1,0,1] op_sel_hi:[1,1,0]
	v_mul_f32_e32 v146, 0.15915494, v197
	v_pk_fma_f16 v142, v141, v141, -2.0 op_sel:[0,1,1] op_sel_hi:[1,1,0]
	v_cvt_scalef32_pk_fp8_f16 v140, v141, 1.0 op_sel:[0,0,1]
	v_cvt_scalef32_pk_fp8_f16 v141, v142, 1.0
	v_pk_fma_f16 v145, v142, v142, -2.0 op_sel:[0,1,1] op_sel_hi:[1,1,0]
	v_add_f32_e32 v142, v144, v144
	v_cvt_pk_f16_f32 v144, v143, v142
	v_lshl_add_u64 v[142:143], v[160:161], 2, s[4:5]
	global_load_dwordx4 v[198:201], v[142:143], off offset:16
	global_load_dwordx4 v[194:197], v[142:143], off offset:3472
	v_cvt_scalef32_pk_fp8_f16 v141, v145, 1.0 op_sel:[0,0,1]
	v_pk_fma_f16 v160, v144, v144, -2.0 op_sel:[1,0,1] op_sel_hi:[1,1,0]
	v_cvt_scalef32_pk_fp8_f16 v143, v144, 1.0
	v_pk_fma_f16 v144, v145, v145, -2.0 op_sel:[0,1,1] op_sel_hi:[1,1,0]
	v_cos_f32_e32 v145, v146
	v_sin_f32_e32 v146, v146
	v_pk_fma_f16 v148, v138, v138, -2.0 op_sel:[0,1,1] op_sel_hi:[1,1,0]
	v_cvt_scalef32_pk_fp8_f16 v136, v139, 1.0
	v_pk_fma_f16 v139, v139, v139, -2.0 op_sel:[0,1,1] op_sel_hi:[1,1,0]
	v_pk_fma_f16 v149, v148, v148, -2.0 op_sel:[0,1,1] op_sel_hi:[1,1,0]
	v_cvt_scalef32_pk_fp8_f16 v142, v144, 1.0
	v_pk_fma_f16 v144, v144, v144, -2.0 op_sel:[0,1,1] op_sel_hi:[1,1,0]
	v_cvt_scalef32_pk_fp8_f16 v137, v138, 1.0 op_sel:[0,0,1]
	v_cvt_scalef32_pk_fp8_f16 v136, v139, 1.0 op_sel:[0,0,1]
	v_pk_fma_f16 v138, v149, v149, -2.0 op_sel:[0,1,1] op_sel_hi:[1,1,0]
	v_cvt_scalef32_pk_fp8_f16 v142, v144, 1.0 op_sel:[0,0,1]
	v_add_f32_e32 v144, v145, v145
	v_cvt_scalef32_pk_fp8_f16 v139, v138, 1.0
	v_pk_fma_f16 v138, v138, v138, -2.0 op_sel:[0,1,1] op_sel_hi:[1,1,0]
	s_waitcnt lgkmcnt(4)
	v_mfma_scale_f32_32x32x64_f8f6f4 v[64:79], v[236:243], v[128:135], v[64:79], v227, v226 op_sel_hi:[0,0,0]
	v_cvt_pk_f16_f32 v144, v146, v144
	v_cvt_scalef32_pk_fp8_f16 v139, v138, 1.0 op_sel:[0,0,1]
	v_pk_fma_f16 v146, v144, v144, -2.0 op_sel:[1,0,1] op_sel_hi:[1,1,0]
	v_cvt_scalef32_pk_fp8_f16 v138, v148, 1.0
	v_cvt_scalef32_pk_fp8_f16 v145, v144, 1.0
	v_pk_fma_f16 v147, v180, v180, -2.0 op_sel:[0,1,1] op_sel_hi:[1,1,0]
	v_pk_fma_f16 v148, v146, v146, -2.0 op_sel:[0,1,1] op_sel_hi:[1,1,0]
	v_cvt_scalef32_pk_fp8_f16 v138, v149, 1.0 op_sel:[0,0,1]
	v_cvt_scalef32_pk_fp8_f16 v144, v147, 1.0
	v_pk_fma_f16 v147, v147, v147, -2.0 op_sel:[0,1,1] op_sel_hi:[1,1,0]
	v_pk_fma_f16 v149, v148, v148, -2.0 op_sel:[0,1,1] op_sel_hi:[1,1,0]
	v_cvt_scalef32_pk_fp8_f16 v145, v146, 1.0 op_sel:[0,0,1]
	v_mfma_scale_f32_32x32x64_f8f6f4 v[80:95], v[236:243], v[152:159], v[80:95], v227, v226 op_sel_hi:[0,0,0]
	v_pk_fma_f16 v146, v149, v149, -2.0 op_sel:[0,1,1] op_sel_hi:[1,1,0]
	v_cvt_scalef32_pk_fp8_f16 v144, v147, 1.0 op_sel:[0,0,1]
	v_cvt_scalef32_pk_fp8_f16 v147, v146, 1.0
	v_pk_fma_f16 v146, v146, v146, -2.0 op_sel:[0,1,1] op_sel_hi:[1,1,0]
	v_sin_f32_e32 v150, v150
	v_cvt_scalef32_pk_fp8_f16 v147, v146, 1.0 op_sel:[0,0,1]
	v_cvt_scalef32_pk_fp8_f16 v146, v148, 1.0
	v_add_f32_e32 v148, v151, v151
	v_mul_f32_e32 v151, 0.15915494, v187
	v_cvt_scalef32_pk_fp8_f16 v146, v149, 1.0 op_sel:[0,0,1]
	v_cvt_pk_f16_f32 v149, v150, v148
	v_cvt_scalef32_pk_fp8_f16 v148, v149, 1.0
	s_waitcnt lgkmcnt(0)
	v_mfma_scale_f32_32x32x64_f8f6f4 v[0:15], v[162:169], v[128:135], v[0:15], v227, v226 op_sel_hi:[0,0,0]
	v_pk_fma_f16 v149, v149, v149, -2.0 op_sel:[1,0,1] op_sel_hi:[1,1,0]
	v_cvt_scalef32_pk_fp8_f16 v143, v160, 1.0 op_sel:[0,0,1]
	v_pk_fma_f16 v150, v149, v149, -2.0 op_sel:[0,1,1] op_sel_hi:[1,1,0]
	v_cvt_scalef32_pk_fp8_f16 v148, v149, 1.0 op_sel:[0,0,1]
	v_cvt_scalef32_pk_fp8_f16 v149, v150, 1.0
	v_mfma_scale_f32_32x32x64_f8f6f4 v[32:47], v[170:177], v[128:135], v[32:47], v227, v226 op_sel_hi:[0,0,0]
	v_cos_f32_e32 v128, v151
	v_sin_f32_e32 v129, v151
	v_pk_fma_f16 v130, v150, v150, -2.0 op_sel:[0,1,1] op_sel_hi:[1,1,0]
	v_add_f32_e32 v128, v128, v128
	v_cvt_pk_f16_f32 v128, v129, v128
	v_pk_fma_f16 v203, v128, v128, -2.0 op_sel:[1,0,1] op_sel_hi:[1,1,0]
	v_cvt_scalef32_pk_fp8_f16 v151, v128, 1.0
	v_pk_fma_f16 v128, v130, v130, -2.0 op_sel:[0,1,1] op_sel_hi:[1,1,0]
	s_nop 0
	v_cvt_scalef32_pk_fp8_f16 v150, v128, 1.0
	v_pk_fma_f16 v128, v128, v128, -2.0 op_sel:[0,1,1] op_sel_hi:[1,1,0]
	v_cvt_scalef32_pk_fp8_f16 v149, v130, 1.0 op_sel:[0,0,1]
	v_cvt_scalef32_pk_fp8_f16 v151, v203, 1.0 op_sel:[0,0,1]
	v_cvt_scalef32_pk_fp8_f16 v150, v128, 1.0 op_sel:[0,0,1]
	v_mfma_scale_f32_32x32x64_f8f6f4 v[48:63], v[170:177], v[152:159], v[48:63], v227, v226 op_sel_hi:[0,0,0]
	v_mfma_scale_f32_32x32x64_f8f6f4 v[16:31], v[162:169], v[152:159], v[16:31], v227, v226 op_sel_hi:[0,0,0]
	v_pk_fma_f16 v130, v160, v160, -2.0 op_sel:[0,1,1] op_sel_hi:[1,1,0]
	s_nop 0
	v_pk_fma_f16 v131, v130, v130, -2.0 op_sel:[0,1,1] op_sel_hi:[1,1,0]
	ds_read_b128 v[152:155], v234 offset:24576
	ds_read_b128 v[156:159], v234 offset:25600
	ds_read_b128 v[162:165], v234 offset:26624
	ds_read_b128 v[166:169], v234 offset:27648
	v_pk_fma_f16 v128, v131, v131, -2.0 op_sel:[0,1,1] op_sel_hi:[1,1,0]
	v_mov_b32_e32 v160, v204
	v_pk_fma_f16 v132, v128, v128, -2.0 op_sel:[0,1,1] op_sel_hi:[1,1,0]
	v_cvt_scalef32_pk_fp8_f16 v129, v128, 1.0
	v_cvt_scalef32_pk_fp8_f16 v129, v132, 1.0 op_sel:[0,0,1]
	v_mul_f32_e32 v132, 0.15915494, v179
	v_sin_f32_e32 v133, v132
	v_cos_f32_e32 v132, v132
	v_cvt_scalef32_pk_fp8_f16 v128, v130, 1.0
	v_cvt_scalef32_pk_fp8_f16 v128, v131, 1.0 op_sel:[0,0,1]
	v_add_f32_e32 v130, v132, v132
	v_cvt_pk_f16_f32 v132, v133, v130
	v_pk_fma_f16 v133, v132, v132, -2.0 op_sel:[1,0,1] op_sel_hi:[1,1,0]
	s_nop 0
	v_pk_fma_f16 v130, v133, v133, -2.0 op_sel:[0,1,1] op_sel_hi:[1,1,0]
	s_waitcnt lgkmcnt(2)
	v_mfma_scale_f32_32x32x64_f8f6f4 v[96:111], v[152:159], v[136:143], v[96:111], v227, v226 op_sel_hi:[0,0,0]
	v_cvt_scalef32_pk_fp8_f16 v131, v130, 1.0
	v_pk_fma_f16 v134, v130, v130, -2.0 op_sel:[0,1,1] op_sel_hi:[1,1,0]
	v_cvt_scalef32_pk_fp8_f16 v130, v132, 1.0
	v_cvt_scalef32_pk_fp8_f16 v131, v134, 1.0 op_sel:[0,0,1]
	v_cvt_scalef32_pk_fp8_f16 v130, v133, 1.0 op_sel:[0,0,1]
	v_pk_fma_f16 v133, v134, v134, -2.0 op_sel:[0,1,1] op_sel_hi:[1,1,0]
	v_mul_f32_e32 v134, 0.15915494, v181
	v_cos_f32_e32 v135, v134
	v_sin_f32_e32 v134, v134
	v_cvt_scalef32_pk_fp8_f16 v132, v133, 1.0
	v_pk_fma_f16 v133, v133, v133, -2.0 op_sel:[0,1,1] op_sel_hi:[1,1,0]
	ds_read_b128 v[170:173], v234 offset:28672
	ds_read_b128 v[174:177], v234 offset:29696
	ds_read_b128 v[236:239], v234 offset:30720
	ds_read_b128 v[240:243], v234 offset:31744
	v_cvt_scalef32_pk_fp8_f16 v132, v133, 1.0 op_sel:[0,0,1]
	v_add_f32_e32 v133, v135, v135
	v_mfma_scale_f32_32x32x64_f8f6f4 v[112:127], v[152:159], v[144:151], v[112:127], v227, v226 op_sel_hi:[0,0,0]
	v_cvt_pk_f16_f32 v152, v134, v133
	v_mul_f32_e32 v153, 0.15915494, v188
	v_lshl_add_u64 v[134:135], v[160:161], 2, s[4:5]
	v_mul_f32_e32 v154, 0.15915494, v189
	global_load_dwordx4 v[178:181], v[134:135], off offset:32
	global_load_dwordx4 v[186:189], v[134:135], off offset:3488
	v_pk_fma_f16 v134, v152, v152, -2.0 op_sel:[1,0,1] op_sel_hi:[1,1,0]
	v_cvt_scalef32_pk_fp8_f16 v133, v152, 1.0
	v_pk_fma_f16 v152, v134, v134, -2.0 op_sel:[0,1,1] op_sel_hi:[1,1,0]
	v_cvt_scalef32_pk_fp8_f16 v133, v134, 1.0 op_sel:[0,0,1]
	v_pk_fma_f16 v155, v152, v152, -2.0 op_sel:[0,1,1] op_sel_hi:[1,1,0]
	s_nop 0
	v_pk_fma_f16 v134, v155, v155, -2.0 op_sel:[0,1,1] op_sel_hi:[1,1,0]
	s_nop 0
	v_pk_fma_f16 v156, v134, v134, -2.0 op_sel:[0,1,1] op_sel_hi:[1,1,0]
	v_cvt_scalef32_pk_fp8_f16 v135, v134, 1.0
	v_cvt_scalef32_pk_fp8_f16 v134, v152, 1.0
	v_pk_fma_f16 v152, v203, v203, -2.0 op_sel:[0,1,1] op_sel_hi:[1,1,0]
	v_cvt_scalef32_pk_fp8_f16 v134, v155, 1.0 op_sel:[0,0,1]
	v_pk_fma_f16 v155, v152, v152, -2.0 op_sel:[0,1,1] op_sel_hi:[1,1,0]
	s_waitcnt lgkmcnt(4)
	v_mfma_scale_f32_32x32x64_f8f6f4 v[64:79], v[162:169], v[136:143], v[64:79], v227, v226 op_sel_hi:[0,0,0]
	v_cvt_scalef32_pk_fp8_f16 v135, v156, 1.0 op_sel:[0,0,1]
	v_pk_fma_f16 v156, v155, v155, -2.0 op_sel:[0,1,1] op_sel_hi:[1,1,0]
	s_nop 0
	v_pk_fma_f16 v157, v156, v156, -2.0 op_sel:[0,1,1] op_sel_hi:[1,1,0]
	v_mfma_scale_f32_32x32x64_f8f6f4 v[80:95], v[162:169], v[144:151], v[80:95], v227, v226 op_sel_hi:[0,0,0]
	v_cvt_scalef32_pk_fp8_f16 v165, v156, 1.0
	v_cos_f32_e32 v156, v153
	v_sin_f32_e32 v153, v153
	v_cvt_scalef32_pk_fp8_f16 v164, v152, 1.0
	v_add_f32_e32 v152, v156, v156
	v_cvt_pk_f16_f32 v152, v153, v152
	v_pk_fma_f16 v153, v152, v152, -2.0 op_sel:[1,0,1] op_sel_hi:[1,1,0]
	v_cvt_scalef32_pk_fp8_f16 v166, v152, 1.0
	v_cvt_scalef32_pk_fp8_f16 v164, v155, 1.0 op_sel:[0,0,1]
	v_pk_fma_f16 v155, v153, v153, -2.0 op_sel:[0,1,1] op_sel_hi:[1,1,0]
	v_cvt_scalef32_pk_fp8_f16 v166, v153, 1.0 op_sel:[0,0,1]
	s_waitcnt lgkmcnt(0)
	v_mfma_scale_f32_32x32x64_f8f6f4 v[0:15], v[236:243], v[136:143], v[0:15], v227, v226 op_sel_hi:[0,0,0]
	v_cos_f32_e32 v153, v154
	v_cvt_scalef32_pk_fp8_f16 v167, v155, 1.0
	v_pk_fma_f16 v155, v155, v155, -2.0 op_sel:[0,1,1] op_sel_hi:[1,1,0]
	v_sin_f32_e32 v154, v154
	v_pk_fma_f16 v152, v155, v155, -2.0 op_sel:[0,1,1] op_sel_hi:[1,1,0]
	s_nop 0
	v_cvt_scalef32_pk_fp8_f16 v168, v152, 1.0
	v_pk_fma_f16 v152, v152, v152, -2.0 op_sel:[0,1,1] op_sel_hi:[1,1,0]
	s_nop 0
	v_cvt_scalef32_pk_fp8_f16 v168, v152, 1.0 op_sel:[0,0,1]
	v_add_f32_e32 v152, v153, v153
	v_cvt_scalef32_pk_fp8_f16 v165, v157, 1.0 op_sel:[0,0,1]
	v_cvt_scalef32_pk_fp8_f16 v167, v155, 1.0 op_sel:[0,0,1]
	v_mfma_scale_f32_32x32x64_f8f6f4 v[32:47], v[170:177], v[136:143], v[32:47], v227, v226 op_sel_hi:[0,0,0]
	v_cvt_pk_f16_f32 v136, v154, v152
	v_cvt_scalef32_pk_fp8_f16 v169, v136, 1.0
	v_pk_fma_f16 v136, v136, v136, -2.0 op_sel:[1,0,1] op_sel_hi:[1,1,0]
	s_nop 0
	v_cvt_scalef32_pk_fp8_f16 v169, v136, 1.0 op_sel:[0,0,1]
	v_pk_fma_f16 v136, v136, v136, -2.0 op_sel:[0,1,1] op_sel_hi:[1,1,0]
	s_nop 0
	v_pk_fma_f16 v137, v136, v136, -2.0 op_sel:[0,1,1] op_sel_hi:[1,1,0]
	s_nop 0
	v_pk_fma_f16 v138, v137, v137, -2.0 op_sel:[0,1,1] op_sel_hi:[1,1,0]
	s_nop 0
	v_pk_fma_f16 v139, v138, v138, -2.0 op_sel:[0,1,1] op_sel_hi:[1,1,0]
	v_mfma_scale_f32_32x32x64_f8f6f4 v[48:63], v[170:177], v[144:151], v[48:63], v227, v226 op_sel_hi:[0,0,0]
	v_cvt_scalef32_pk_fp8_f16 v171, v138, 1.0
	v_cvt_scalef32_pk_fp8_f16 v170, v136, 1.0
	v_cvt_scalef32_pk_fp8_f16 v171, v139, 1.0 op_sel:[0,0,1]
	v_cvt_scalef32_pk_fp8_f16 v170, v137, 1.0 op_sel:[0,0,1]
	v_mfma_scale_f32_32x32x64_f8f6f4 v[16:31], v[236:243], v[144:151], v[16:31], v227, v226 op_sel_hi:[0,0,0]
	v_mul_f32_e32 v152, 0.15915494, v225
	ds_read_b128 v[136:139], v234 offset:32768
	ds_read_b128 v[140:143], v234 offset:33792
	v_cos_f32_e32 v153, v152
	v_sin_f32_e32 v152, v152
	v_mov_b32_e32 v205, v161
	s_waitcnt lgkmcnt(0)
	v_mfma_scale_f32_32x32x64_f8f6f4 v[96:111], v[136:143], v[128:135], v[96:111], v227, v226 op_sel_hi:[0,0,0]
	v_add_f32_e32 v153, v153, v153
	v_cvt_pk_f16_f32 v158, v152, v153
	v_mov_b32_e32 v203, v161
	v_cndmask_b32_e64 v162, 0, v222, s[0:1]
	v_mul_f32_e32 v163, 0.15915494, v223
	v_pk_fma_f16 v159, v158, v158, -2.0 op_sel:[1,0,1] op_sel_hi:[1,1,0]
	v_cndmask_b32_e64 v172, 0, v224, s[0:1]
	v_pk_fma_f16 v156, v159, v159, -2.0 op_sel:[0,1,1] op_sel_hi:[1,1,0]
	s_nop 0
	v_pk_fma_f16 v160, v156, v156, -2.0 op_sel:[0,1,1] op_sel_hi:[1,1,0]
	v_cvt_scalef32_pk_fp8_f16 v157, v156, 1.0
	v_cvt_scalef32_pk_fp8_f16 v156, v158, 1.0
	v_cvt_scalef32_pk_fp8_f16 v156, v159, 1.0 op_sel:[0,0,1]
	v_mfma_scale_f32_32x32x64_f8f6f4 v[112:127], v[136:143], v[164:171], v[112:127], v227, v226 op_sel_hi:[0,0,0]
	ds_read_b128 v[136:139], v234 offset:34816
	ds_read_b128 v[140:143], v234 offset:35840
	ds_read_b128 v[144:147], v234 offset:36864
	ds_read_b128 v[148:151], v234 offset:37888
	ds_read_b128 v[236:239], v234 offset:38912
	ds_read_b128 v[240:243], v234 offset:39936
	v_lshl_add_u64 v[152:153], v[204:205], 2, s[4:5]
	v_lshl_add_u64 v[154:155], v[202:203], 2, s[4:5]
	global_load_dword v225, v[152:153], off offset:48
	global_load_dword v222, v[154:155], off
	global_load_dword v224, v[154:155], off offset:3456
	global_load_dword v223, v[152:153], off offset:3504
	v_cvt_scalef32_pk_fp8_f16 v157, v160, 1.0 op_sel:[0,0,1]
	s_waitcnt lgkmcnt(4)
	v_mfma_scale_f32_32x32x64_f8f6f4 v[64:79], v[136:143], v[128:135], v[64:79], v227, v226 op_sel_hi:[0,0,0]
	v_mfma_scale_f32_32x32x64_f8f6f4 v[80:95], v[136:143], v[164:171], v[80:95], v227, v226 op_sel_hi:[0,0,0]
	v_mul_f32_e32 v136, v207, v208
	v_fma_f32 v137, v208, v208, -2.0
	v_cndmask_b32_e64 v138, v137, v136, s[0:1]
	v_mul_f32_e32 v136, v136, v137
	v_fma_f32 v137, v137, v137, -2.0
	v_cndmask_b32_e64 v139, v137, v136, s[0:1]
	v_cvt_pk_fp8_f32 v159, v138, v139
	v_mul_f32_e32 v136, v136, v137
	v_fma_f32 v137, v137, v137, -2.0
	v_cndmask_b32_e64 v136, v137, v136, s[0:1]
	v_cvt_pk_fp8_f32 v159, v136, v162 op_sel:[0,0,1]
	v_pk_fma_f16 v136, v160, v160, -2.0 op_sel:[0,1,1] op_sel_hi:[1,1,0]
	v_mov_b32_e32 v160, v161
	v_pk_fma_f16 v137, v136, v136, -2.0 op_sel:[0,1,1] op_sel_hi:[1,1,0]
	v_cvt_scalef32_pk_fp8_f16 v158, v136, 1.0
	v_cos_f32_e32 v136, v163
	v_cvt_scalef32_pk_fp8_f16 v158, v137, 1.0 op_sel:[0,0,1]
	v_sin_f32_e32 v137, v163
	s_waitcnt lgkmcnt(0)
	v_mfma_scale_f32_32x32x64_f8f6f4 v[0:15], v[236:243], v[128:135], v[0:15], v227, v226 op_sel_hi:[0,0,0]
	v_add_f32_e32 v136, v136, v136
	v_mov_b32_e32 v162, v161
	v_cvt_pk_f16_f32 v138, v137, v136
	v_pk_fma_f16 v139, v138, v138, -2.0 op_sel:[1,0,1] op_sel_hi:[1,1,0]
	s_nop 0
	v_pk_fma_f16 v136, v139, v139, -2.0 op_sel:[0,1,1] op_sel_hi:[1,1,0]
	v_mov_b32_e32 v163, v161
	v_pk_fma_f16 v140, v136, v136, -2.0 op_sel:[0,1,1] op_sel_hi:[1,1,0]
	v_cvt_scalef32_pk_fp8_f16 v137, v136, 1.0
	v_cvt_scalef32_pk_fp8_f16 v136, v138, 1.0
	v_cvt_scalef32_pk_fp8_f16 v136, v139, 1.0 op_sel:[0,0,1]
	v_mul_f32_e32 v138, v209, v210
	v_fma_f32 v139, v210, v210, -2.0
	v_cndmask_b32_e64 v141, v139, v138, s[0:1]
	v_mul_f32_e32 v138, v138, v139
	v_fma_f32 v142, v139, v139, -2.0
	v_cndmask_b32_e64 v143, v142, v138, s[0:1]
	v_cvt_pk_fp8_f32 v139, v141, v143
	v_mfma_scale_f32_32x32x64_f8f6f4 v[32:47], v[144:151], v[128:135], v[32:47], v227, v226 op_sel_hi:[0,0,0]
	v_mul_f32_e32 v128, v138, v142
	v_fma_f32 v129, v142, v142, -2.0
	v_cndmask_b32_e64 v128, v129, v128, s[0:1]
	v_cvt_pk_fp8_f32 v139, v128, v172 op_sel:[0,0,1]
	v_pk_fma_f16 v128, v140, v140, -2.0 op_sel:[0,1,1] op_sel_hi:[1,1,0]
	s_nop 0
	v_cvt_scalef32_pk_fp8_f16 v138, v128, 1.0
	v_pk_fma_f16 v128, v128, v128, -2.0 op_sel:[0,1,1] op_sel_hi:[1,1,0]
	v_cvt_scalef32_pk_fp8_f16 v137, v140, 1.0 op_sel:[0,0,1]
	v_cvt_scalef32_pk_fp8_f16 v138, v128, 1.0 op_sel:[0,0,1]
	v_mov_b32_e32 v140, v161
	v_mov_b32_e32 v141, v161
	v_mov_b32_e32 v142, v161
	v_mov_b32_e32 v143, v161
	v_mfma_scale_f32_32x32x64_f8f6f4 v[48:63], v[144:151], v[164:171], v[48:63], v227, v226 op_sel_hi:[0,0,0]
	v_mfma_scale_f32_32x32x64_f8f6f4 v[16:31], v[236:243], v[164:171], v[16:31], v227, v226 op_sel_hi:[0,0,0]
	ds_read_b128 v[128:131], v234 offset:40960
	ds_read_b128 v[132:135], v234 offset:41984
	s_waitcnt lgkmcnt(0)
	v_mfma_scale_f32_32x32x64_f8f6f4 v[96:111], v[128:135], v[156:163], v[96:111], v227, v226 op_sel_hi:[0,0,0]
	v_mfma_scale_f32_32x32x64_f8f6f4 v[112:127], v[128:135], v[136:143], v[112:127], v227, v226 op_sel_hi:[0,0,0]
	ds_read_b128 v[128:131], v234 offset:43008
	ds_read_b128 v[132:135], v234 offset:44032
	s_waitcnt lgkmcnt(0)
	v_mfma_scale_f32_32x32x64_f8f6f4 v[64:79], v[128:135], v[156:163], v[64:79], v227, v226 op_sel_hi:[0,0,0]
	v_mfma_scale_f32_32x32x64_f8f6f4 v[80:95], v[128:135], v[136:143], v[80:95], v227, v226 op_sel_hi:[0,0,0]
	ds_read_b128 v[128:131], v234 offset:45056
	ds_read_b128 v[132:135], v234 offset:46080
	s_waitcnt lgkmcnt(0)
	v_mfma_scale_f32_32x32x64_f8f6f4 v[32:47], v[128:135], v[156:163], v[32:47], v227, v226 op_sel_hi:[0,0,0]
	v_mfma_scale_f32_32x32x64_f8f6f4 v[48:63], v[128:135], v[136:143], v[48:63], v227, v226 op_sel_hi:[0,0,0]
	ds_read_b128 v[128:131], v234 offset:47104
	ds_read_b128 v[132:135], v234 offset:48128
	ds_read_b128 v[174:177], v234 offset:49152
	ds_read_b128 v[208:211], v234 offset:50176
	ds_read_b128 v[212:215], v234 offset:53248
	ds_read_b128 v[236:239], v234 offset:54272
	s_waitcnt lgkmcnt(4)
	v_mfma_scale_f32_32x32x64_f8f6f4 v[0:15], v[128:135], v[156:163], v[0:15], v227, v226 op_sel_hi:[0,0,0]
	v_mfma_scale_f32_32x32x64_f8f6f4 v[16:31], v[128:135], v[136:143], v[16:31], v227, v226 op_sel_hi:[0,0,0]
	v_cvt_pk_bf16_f32 v162, v96, v97 clamp
	v_cvt_pk_bf16_f32 v163, v98, v99 clamp
	v_cvt_pk_bf16_f32 v164, v100, v101 clamp
	v_cvt_pk_bf16_f32 v165, v102, v103 clamp
	v_cvt_pk_bf16_f32 v166, v112, v113 clamp
	v_cvt_pk_bf16_f32 v167, v114, v115 clamp
	v_cvt_pk_bf16_f32 v168, v116, v117 clamp
	v_cvt_pk_bf16_f32 v169, v118, v119 clamp
	v_cvt_pk_bf16_f32 v170, v104, v105 clamp
	v_cvt_pk_bf16_f32 v171, v106, v107 clamp
	v_cvt_pk_bf16_f32 v172, v108, v109 clamp
	v_add_u32_e32 v128, 0, v206
	v_cvt_pk_bf16_f32 v173, v110, v111 clamp
	v_add_u32_e32 v235, 0x18000, v128
	v_cvt_pk_bf16_f32 v202, v120, v121 clamp
	ds_read_b128 v[128:131], v235
	ds_read_b128 v[132:135], v235 offset:32
	ds_read_b128 v[136:139], v235 offset:64
	ds_read_b128 v[140:143], v235 offset:96
	v_cvt_pk_bf16_f32 v203, v122, v123 clamp
	ds_read_b128 v[96:99], v235 offset:128
	ds_read_b128 v[100:103], v235 offset:160
	ds_read_b128 v[104:107], v235 offset:192
	ds_read_b128 v[108:111], v235 offset:224
	v_cvt_pk_bf16_f32 v204, v124, v125 clamp
	v_cvt_pk_bf16_f32 v64, v64, v65
	s_waitcnt lgkmcnt(4)
	v_mfma_f32_32x32x16_bf16 v[144:159], v[174:177], v[166:169], v[128:143]
	v_cvt_pk_bf16_f32 v205, v126, v127 clamp
	ds_read_b128 v[240:243], v234 offset:57344
	ds_read_b128 v[244:247], v234 offset:58368
	ds_read_b128 v[248:251], v234 offset:61440
	ds_read_b128 v[252:255], v234 offset:62464
	v_cvt_pk_bf16_f32 v65, v74, v75 clamp
	v_cndmask_b32_e64 v230, v230, 0, s[14:15]
	v_mfma_f32_32x32x16_bf16 v[128:143], v[174:177], v[162:165], v[128:143]
	v_pk_max_i16 v174, v64, 0
	v_cvt_pk_bf16_f32 v175, v66, v67 clamp
	v_cvt_pk_bf16_f32 v176, v68, v69 clamp
	v_cvt_pk_bf16_f32 v177, v70, v71 clamp
	s_waitcnt lgkmcnt(4)
	v_mfma_f32_32x32x16_bf16 v[112:127], v[208:211], v[166:169], v[96:111]
	v_cvt_pk_bf16_f32 v80, v80, v81 clamp
	v_cvt_pk_bf16_f32 v81, v82, v83 clamp
	v_cvt_pk_bf16_f32 v82, v84, v85 clamp
	v_cvt_pk_bf16_f32 v83, v86, v87 clamp
	v_mfma_f32_32x32x16_bf16 v[96:111], v[208:211], v[162:165], v[96:111]
	v_cvt_pk_bf16_f32 v64, v72, v73 clamp
	v_cvt_pk_bf16_f32 v66, v76, v77 clamp
	v_cvt_pk_bf16_f32 v67, v78, v79 clamp
	v_cvt_pk_bf16_f32 v68, v88, v89 clamp
	v_cvt_pk_bf16_f32 v69, v90, v91 clamp
	v_cvt_pk_bf16_f32 v70, v92, v93 clamp
	v_cvt_pk_bf16_f32 v71, v94, v95 clamp
	v_add_u32_e32 v160, 0x14000, v234
	v_mfma_f32_32x32x16_bf16 v[128:143], v[212:215], v[170:173], v[128:143]
	v_mfma_f32_32x32x16_bf16 v[144:159], v[212:215], v[202:205], v[144:159]
	v_mfma_f32_32x32x16_bf16 v[96:111], v[236:239], v[170:173], v[96:111]
	v_mfma_f32_32x32x16_bf16 v[112:127], v[236:239], v[202:205], v[112:127]
	v_cvt_pk_bf16_f32 v76, v32, v33 clamp
	v_cvt_pk_bf16_f32 v77, v34, v35 clamp
	v_cvt_pk_bf16_f32 v78, v36, v37 clamp
	v_cvt_pk_bf16_f32 v79, v38, v39 clamp
	v_cvt_pk_bf16_f32 v88, v48, v49 clamp
	v_cvt_pk_bf16_f32 v89, v50, v51 clamp
	v_cvt_pk_bf16_f32 v90, v52, v53 clamp
	v_cvt_pk_bf16_f32 v91, v54, v55 clamp
	s_waitcnt lgkmcnt(3)
	v_mfma_f32_32x32x16_bf16 v[128:143], v[240:243], v[174:177], v[128:143]
	v_cvt_pk_bf16_f32 v72, v40, v41 clamp
	v_cvt_pk_bf16_f32 v73, v42, v43 clamp
	v_cvt_pk_bf16_f32 v74, v44, v45 clamp
	v_mfma_f32_32x32x16_bf16 v[144:159], v[240:243], v[80:83], v[144:159]
	ds_read_b128 v[92:95], v233 offset:16384
	ds_read_b128 v[208:211], v233 offset:17408
	ds_read_b128 v[236:239], v233 offset:20480
	ds_read_b128 v[240:243], v233 offset:21504
	v_cvt_pk_bf16_f32 v75, v46, v47 clamp
	v_cvt_pk_bf16_f32 v84, v56, v57 clamp
	v_cvt_pk_bf16_f32 v85, v58, v59 clamp
	s_waitcnt lgkmcnt(6)
	v_mfma_f32_32x32x16_bf16 v[96:111], v[244:247], v[174:177], v[96:111]
	v_cvt_pk_bf16_f32 v86, v60, v61 clamp
	v_cvt_pk_bf16_f32 v87, v62, v63 clamp
	v_mfma_f32_32x32x16_bf16 v[112:127], v[244:247], v[80:83], v[112:127]
	s_waitcnt lgkmcnt(5)
	v_mfma_f32_32x32x16_bf16 v[128:143], v[248:251], v[64:67], v[128:143]
	v_mfma_f32_32x32x16_bf16 v[144:159], v[248:251], v[68:71], v[144:159]
	s_waitcnt lgkmcnt(4)
	v_mfma_f32_32x32x16_bf16 v[96:111], v[252:255], v[64:67], v[96:111]
	v_mfma_f32_32x32x16_bf16 v[112:127], v[252:255], v[68:71], v[112:127]
	v_cvt_pk_bf16_f32 v206, v0, v1 clamp
	v_cvt_pk_bf16_f32 v207, v2, v3 clamp
	v_cvt_pk_bf16_f32 v0, v4, v5
	s_waitcnt lgkmcnt(2)
	v_mfma_f32_32x32x16_bf16 v[96:111], v[208:211], v[76:79], v[96:111]
	ds_read_b128 v[32:35], v233 offset:24576
	ds_read_b128 v[36:39], v233 offset:25600
	ds_read_b128 v[40:43], v233 offset:28672
	ds_read_b128 v[44:47], v233 offset:29696
	v_mfma_f32_32x32x16_bf16 v[112:127], v[208:211], v[88:91], v[112:127]
	v_pk_max_i16 v208, v0, 0
	v_cvt_pk_bf16_f32 v209, v6, v7 clamp
	v_cvt_pk_bf16_f32 v214, v16, v17 clamp
	v_cvt_pk_bf16_f32 v215, v18, v19 clamp
	v_cvt_pk_bf16_f32 v216, v20, v21 clamp
	v_cvt_pk_bf16_f32 v217, v22, v23 clamp
	v_mfma_f32_32x32x16_bf16 v[128:143], v[92:95], v[76:79], v[128:143]
	v_cvt_pk_bf16_f32 v0, v8, v9
	v_mfma_f32_32x32x16_bf16 v[144:159], v[92:95], v[88:91], v[144:159]
	v_pk_max_i16 v92, v0, 0
	v_cvt_pk_bf16_f32 v93, v10, v11 clamp
	v_cvt_pk_bf16_f32 v94, v12, v13 clamp
	v_cvt_pk_bf16_f32 v95, v14, v15 clamp
	v_cvt_pk_bf16_f32 v210, v24, v25 clamp
	v_cvt_pk_bf16_f32 v211, v26, v27 clamp
	v_cvt_pk_bf16_f32 v212, v28, v29 clamp
	v_cvt_pk_bf16_f32 v213, v30, v31 clamp
	s_waitcnt lgkmcnt(5)
	v_mfma_f32_32x32x16_bf16 v[128:143], v[236:239], v[72:75], v[128:143]
	v_mfma_f32_32x32x16_bf16 v[144:159], v[236:239], v[84:87], v[144:159]
	s_waitcnt lgkmcnt(4)
	v_mfma_f32_32x32x16_bf16 v[96:111], v[240:243], v[72:75], v[96:111]
	v_mfma_f32_32x32x16_bf16 v[112:127], v[240:243], v[84:87], v[112:127]
	s_waitcnt lgkmcnt(3)
	v_mfma_f32_32x32x16_bf16 v[128:143], v[32:35], v[206:209], v[128:143]
	ds_read_b128 v[0:3], v234 offset:51200
	ds_read_b128 v[236:239], v234 offset:52224
	ds_read_b128 v[240:243], v234 offset:55296
	ds_read_b128 v[244:247], v234 offset:56320
	v_mfma_f32_32x32x16_bf16 v[144:159], v[32:35], v[214:217], v[144:159]
	s_waitcnt lgkmcnt(6)
	v_mfma_f32_32x32x16_bf16 v[96:111], v[36:39], v[206:209], v[96:111]
	v_mfma_f32_32x32x16_bf16 v[112:127], v[36:39], v[214:217], v[112:127]
	s_waitcnt lgkmcnt(5)
	v_mfma_f32_32x32x16_bf16 v[128:143], v[40:43], v[92:95], v[128:143]
	v_mfma_f32_32x32x16_bf16 v[144:159], v[40:43], v[210:213], v[144:159]
	s_waitcnt lgkmcnt(4)
	v_mfma_f32_32x32x16_bf16 v[96:111], v[44:47], v[92:95], v[96:111]
	v_mfma_f32_32x32x16_bf16 v[112:127], v[44:47], v[210:213], v[112:127]
	ds_read_b128 v[32:35], v235 offset:256
	ds_read_b128 v[36:39], v235 offset:288
	ds_read_b128 v[40:43], v235 offset:320
	ds_read_b128 v[44:47], v235 offset:352
	s_nop 3
	v_cvt_pk_bf16_f32 v128, v128, v129 clamp
	v_cvt_pk_bf16_f32 v129, v130, v131 clamp
	v_cvt_pk_bf16_f32 v130, v132, v133 clamp
	v_cvt_pk_bf16_f32 v131, v134, v135 clamp
	s_waitcnt lgkmcnt(0)
	v_mfma_f32_32x32x16_bf16 v[48:63], v[0:3], v[166:169], v[32:47]
	v_cvt_pk_bf16_f32 v132, v144, v145 clamp
	v_cvt_pk_bf16_f32 v133, v146, v147 clamp
	v_cvt_pk_bf16_f32 v134, v148, v149 clamp
	v_cvt_pk_bf16_f32 v135, v150, v151 clamp
	v_mfma_f32_32x32x16_bf16 v[32:47], v[0:3], v[162:165], v[32:47]
	ds_read_b128 v[0:3], v235 offset:384
	ds_read_b128 v[4:7], v235 offset:416
	ds_read_b128 v[8:11], v235 offset:448
	ds_read_b128 v[12:15], v235 offset:480
	s_waitcnt lgkmcnt(0)
	v_mfma_f32_32x32x16_bf16 v[16:31], v[236:239], v[166:169], v[0:15]
	v_mfma_f32_32x32x16_bf16 v[0:15], v[236:239], v[162:165], v[0:15]
	ds_read_b128 v[162:165], v234 offset:59392
	ds_read_b128 v[166:169], v234 offset:60416
	ds_read_b128 v[236:239], v234 offset:63488
	ds_read_b128 v[248:251], v234 offset:64512
	v_mfma_f32_32x32x16_bf16 v[0:15], v[244:247], v[170:173], v[0:15]
	v_mfma_f32_32x32x16_bf16 v[32:47], v[240:243], v[170:173], v[32:47]
	v_mfma_f32_32x32x16_bf16 v[48:63], v[240:243], v[202:205], v[48:63]
	v_mfma_f32_32x32x16_bf16 v[16:31], v[244:247], v[202:205], v[16:31]
	s_waitcnt lgkmcnt(2)
	v_mfma_f32_32x32x16_bf16 v[0:15], v[166:169], v[174:177], v[0:15]
	v_cvt_pk_bf16_f32 v136, v136, v137 clamp
	v_cvt_pk_bf16_f32 v137, v138, v139 clamp
	v_cvt_pk_bf16_f32 v138, v140, v141 clamp
	v_cvt_pk_bf16_f32 v139, v142, v143 clamp
	v_cvt_pk_bf16_f32 v140, v152, v153 clamp
	v_mfma_f32_32x32x16_bf16 v[32:47], v[162:165], v[174:177], v[32:47]
	v_mfma_f32_32x32x16_bf16 v[48:63], v[162:165], v[80:83], v[48:63]
	v_mfma_f32_32x32x16_bf16 v[16:31], v[166:169], v[80:83], v[16:31]
	ds_read_b128 v[80:83], v233 offset:18432
	ds_read_b128 v[144:147], v233 offset:19456
	ds_read_b128 v[148:151], v233 offset:22528
	ds_read_b128 v[162:165], v233 offset:23552
	s_waitcnt lgkmcnt(4)
	v_mfma_f32_32x32x16_bf16 v[0:15], v[248:251], v[64:67], v[0:15]
	v_mfma_f32_32x32x16_bf16 v[32:47], v[236:239], v[64:67], v[32:47]
	v_cvt_pk_bf16_f32 v141, v154, v155 clamp
	v_cvt_pk_bf16_f32 v142, v156, v157 clamp
	v_cvt_pk_bf16_f32 v143, v158, v159 clamp
	v_mfma_f32_32x32x16_bf16 v[48:63], v[236:239], v[68:71], v[48:63]
	v_mfma_f32_32x32x16_bf16 v[16:31], v[248:251], v[68:71], v[16:31]
	s_waitcnt lgkmcnt(2)
	v_mfma_f32_32x32x16_bf16 v[0:15], v[144:147], v[76:79], v[0:15]
	v_mfma_f32_32x32x16_bf16 v[32:47], v[80:83], v[76:79], v[32:47]
	v_mfma_f32_32x32x16_bf16 v[48:63], v[80:83], v[88:91], v[48:63]
	ds_read_b128 v[64:67], v233 offset:26624
	ds_read_b128 v[68:71], v233 offset:27648
	ds_read_b128 v[76:79], v233 offset:30720
	ds_read_b128 v[80:83], v233 offset:31744
	v_mfma_f32_32x32x16_bf16 v[16:31], v[144:147], v[88:91], v[16:31]
	v_cvt_pk_bf16_f32 v96, v96, v97 clamp
	v_cvt_pk_bf16_f32 v97, v98, v99 clamp
	v_cvt_pk_bf16_f32 v98, v100, v101 clamp
	v_cvt_pk_bf16_f32 v99, v102, v103 clamp
	s_waitcnt lgkmcnt(4)
	v_mfma_f32_32x32x16_bf16 v[0:15], v[162:165], v[72:75], v[0:15]
	v_cvt_pk_bf16_f32 v100, v112, v113 clamp
	v_mfma_f32_32x32x16_bf16 v[32:47], v[148:151], v[72:75], v[32:47]
	v_cvt_pk_bf16_f32 v101, v114, v115 clamp
	v_cvt_pk_bf16_f32 v102, v116, v117 clamp
	v_cvt_pk_bf16_f32 v103, v118, v119 clamp
	v_mfma_f32_32x32x16_bf16 v[48:63], v[148:151], v[84:87], v[48:63]
	v_mfma_f32_32x32x16_bf16 v[16:31], v[162:165], v[84:87], v[16:31]
	s_waitcnt lgkmcnt(2)
	v_mfma_f32_32x32x16_bf16 v[0:15], v[68:71], v[206:209], v[0:15]
	ds_read_b128 v[84:87], v160
	ds_read_b128 v[112:115], v160 offset:1024
	ds_read_b128 v[116:119], v160 offset:2048
	ds_read_b128 v[144:147], v160 offset:3072
	v_mfma_f32_32x32x16_bf16 v[32:47], v[64:67], v[206:209], v[32:47]
	v_mfma_f32_32x32x16_bf16 v[48:63], v[64:67], v[214:217], v[48:63]
	v_cvt_pk_bf16_f32 v104, v104, v105 clamp
	v_cvt_pk_bf16_f32 v105, v106, v107 clamp
	v_cvt_pk_bf16_f32 v106, v108, v109 clamp
	v_cvt_pk_bf16_f32 v107, v110, v111 clamp
	v_mfma_f32_32x32x16_bf16 v[16:31], v[68:71], v[214:217], v[16:31]
	v_cvt_pk_bf16_f32 v108, v120, v121 clamp
	v_cvt_pk_bf16_f32 v109, v122, v123 clamp
	v_cvt_pk_bf16_f32 v110, v124, v125 clamp
	s_waitcnt lgkmcnt(4)
	v_mfma_f32_32x32x16_bf16 v[0:15], v[80:83], v[92:95], v[0:15]
	v_cvt_pk_bf16_f32 v111, v126, v127 clamp
	v_mfma_f32_32x32x16_bf16 v[32:47], v[76:79], v[92:95], v[32:47]
	v_mfma_f32_32x32x16_bf16 v[48:63], v[76:79], v[210:213], v[48:63]
	v_mfma_f32_32x32x16_bf16 v[16:31], v[80:83], v[210:213], v[16:31]
	s_waitcnt lgkmcnt(3)
	v_mfma_f32_32x32x16_bf16 v[64:79], v[84:87], v[128:131], 0
	s_nop 7
	v_cvt_pk_bf16_f32 v32, v32, v33 clamp
	v_cvt_pk_bf16_f32 v33, v34, v35 clamp
	v_cvt_pk_bf16_f32 v34, v36, v37 clamp
	v_cvt_pk_bf16_f32 v35, v38, v39 clamp
	v_mfma_f32_32x32x16_bf16 v[80:95], v[84:87], v[132:135], 0
	v_cvt_pk_bf16_f32 v48, v48, v49 clamp
	v_cvt_pk_bf16_f32 v49, v50, v51 clamp
	v_cvt_pk_bf16_f32 v50, v52, v53 clamp
	v_cvt_pk_bf16_f32 v51, v54, v55 clamp
	s_waitcnt lgkmcnt(2)
	v_mfma_f32_32x32x16_bf16 v[64:79], v[112:115], v[136:139], v[64:79]
	v_cvt_pk_bf16_f32 v40, v40, v41 clamp
	v_cvt_pk_bf16_f32 v41, v42, v43 clamp
	v_cvt_pk_bf16_f32 v42, v44, v45 clamp
	v_cvt_pk_bf16_f32 v43, v46, v47 clamp
	v_mfma_f32_32x32x16_bf16 v[80:95], v[112:115], v[140:143], v[80:95]
	v_cvt_pk_bf16_f32 v52, v56, v57
	v_cvt_pk_bf16_f32 v53, v58, v59
	v_cvt_pk_bf16_f32 v54, v60, v61
	v_cvt_pk_bf16_f32 v55, v62, v63
	s_waitcnt lgkmcnt(1)
	v_mfma_f32_32x32x16_bf16 v[64:79], v[116:119], v[96:99], v[64:79]
	ds_read_b128 v[36:39], v160 offset:4096
	ds_read_b128 v[96:99], v160 offset:5120
	v_cvt_pk_bf16_f32 v0, v0, v1 clamp
	v_cvt_pk_bf16_f32 v1, v2, v3 clamp
	v_cvt_pk_bf16_f32 v2, v4, v5 clamp
	v_cvt_pk_bf16_f32 v3, v6, v7 clamp
	v_mfma_f32_32x32x16_bf16 v[80:95], v[116:119], v[100:103], v[80:95]
	ds_read_b128 v[4:7], v160 offset:7168
	v_cvt_pk_bf16_f32 v12, v12, v13
	v_cvt_pk_bf16_f32 v13, v14, v15
	v_cvt_pk_bf16_f32 v24, v24, v25
	v_cvt_pk_bf16_f32 v25, v26, v27
	s_waitcnt lgkmcnt(3)
	v_mfma_f32_32x32x16_bf16 v[64:79], v[144:147], v[104:107], v[64:79]
	v_cvt_pk_bf16_f32 v26, v28, v29
	v_cvt_pk_bf16_f32 v27, v30, v31
	v_cndmask_b32_e64 v219, v219, 0, s[14:15]
	v_cndmask_b32_e64 v218, v218, 0, s[14:15]
	v_mfma_f32_32x32x16_bf16 v[80:95], v[144:147], v[108:111], v[80:95]
	s_waitcnt lgkmcnt(2)
	v_mfma_f32_32x32x16_bf16 v[64:79], v[36:39], v[32:35], v[64:79]
	v_cvt_pk_bf16_f32 v34, v20, v21
	v_cvt_pk_bf16_f32 v35, v22, v23
	ds_read_b128 v[20:23], v160 offset:6144
	v_cvt_pk_bf16_f32 v32, v16, v17
	v_cvt_pk_bf16_f32 v33, v18, v19
	v_pk_max_i16 v16, v52, 0
	v_pk_max_i16 v17, v53, 0
	v_mfma_f32_32x32x16_bf16 v[80:95], v[36:39], v[48:51], v[80:95]
	v_pk_max_i16 v18, v54, 0
	v_pk_max_i16 v19, v55, 0
	s_waitcnt lgkmcnt(2)
	v_mfma_f32_32x32x16_bf16 v[64:79], v[96:99], v[40:43], v[64:79]
	v_mfma_f32_32x32x16_bf16 v[80:95], v[96:99], v[16:19], v[80:95]
	v_cvt_pk_bf16_f32 v16, v8, v9
	v_cvt_pk_bf16_f32 v17, v10, v11
	v_pk_max_i16 v8, v24, 0
	v_pk_max_i16 v9, v25, 0
	v_pk_max_i16 v10, v26, 0
	v_pk_max_i16 v11, v27, 0
	s_waitcnt lgkmcnt(0)
	v_mfma_f32_32x32x16_bf16 v[64:79], v[20:23], v[0:3], v[64:79]
	v_pk_max_i16 v0, v32, 0
	v_pk_max_i16 v1, v33, 0
	v_pk_max_i16 v2, v34, 0
	v_pk_max_i16 v3, v35, 0
	s_nop 1
	v_mfma_f32_32x32x16_bf16 v[80:95], v[20:23], v[0:3], v[80:95]
	v_pk_max_i16 v0, v16, 0
	v_pk_max_i16 v1, v17, 0
	v_pk_max_i16 v2, v12, 0
	v_pk_max_i16 v3, v13, 0
	s_nop 1
	v_mfma_f32_32x32x16_bf16 v[64:79], v[4:7], v[0:3], v[64:79]
	v_mfma_f32_32x32x16_bf16 v[80:95], v[4:7], v[8:11], v[80:95]
	s_waitcnt vmcnt(10)
	s_nop 7
	s_nop 2
	v_permlane32_swap_b32_e32 v64, v80
	v_permlane32_swap_b32_e32 v65, v81
	v_permlane32_swap_b32_e32 v66, v82
	s_nop 0
	v_add_f32_e32 v3, s10, v64
	v_add_f32_e32 v4, s11, v65
	v_add_f32_e32 v5, s18, v66
	v_mul_f32_e32 v3, 0xbfb8aa3b, v3
	v_mul_f32_e32 v4, 0xbfb8aa3b, v4
	v_mul_f32_e32 v5, 0xbfb8aa3b, v5
	v_exp_f32_e32 v3, v3
	v_exp_f32_e32 v4, v4
	v_exp_f32_e32 v5, v5
	v_add_f32_e32 v3, 1.0, v3
	v_add_f32_e32 v4, 1.0, v4
	v_add_f32_e32 v5, 1.0, v5
	v_rcp_f32_e32 v3, v3
	v_rcp_f32_e32 v4, v4
	v_rcp_f32_e32 v5, v5
	v_fmac_f32_e32 v218, v232, v3
	v_fmac_f32_e32 v219, v232, v4
	v_fmac_f32_e32 v230, v232, v5
	s_andn2_b64 vcc, exec, s[12:13]
	s_cbranch_vccnz .LBB1_6
	v_and_b32_e32 v1, 64, v229
	v_xor_b32_e32 v0, 32, v229
	v_add_u32_e32 v2, 64, v1
	v_cmp_lt_i32_e32 vcc, v0, v2
	s_nop 1
	v_cndmask_b32_e32 v0, v229, v0, vcc
	v_lshlrev_b32_e32 v0, 2, v0
	s_waitcnt lgkmcnt(0)
	ds_bpermute_b32 v1, v0, v230
	v_xor_b32_e32 v3, 16, v229
	v_cmp_lt_i32_e32 vcc, v3, v2
	ds_bpermute_b32 v4, v0, v218
	ds_bpermute_b32 v5, v0, v219
	v_cndmask_b32_e32 v3, v229, v3, vcc
	v_lshlrev_b32_e32 v3, 2, v3
	s_waitcnt lgkmcnt(2)
	v_add_f32_e32 v1, v230, v1
	ds_bpermute_b32 v6, v3, v1
	v_xor_b32_e32 v0, 8, v229
	v_cmp_lt_i32_e32 vcc, v0, v2
	v_xor_b32_e32 v9, 4, v229
	s_waitcnt lgkmcnt(0)
	v_add_f32_e32 v6, v1, v6
	v_cndmask_b32_e32 v0, v229, v0, vcc
	v_lshlrev_b32_e32 v7, 2, v0
	v_pk_add_f32 v[0:1], v[218:219], v[4:5]
	ds_bpermute_b32 v4, v3, v0
	ds_bpermute_b32 v5, v3, v1
	ds_bpermute_b32 v8, v7, v6
	v_cmp_lt_i32_e32 vcc, v9, v2
	s_waitcnt lgkmcnt(1)
	v_pk_add_f32 v[0:1], v[0:1], v[4:5]
	ds_bpermute_b32 v4, v7, v0
	ds_bpermute_b32 v5, v7, v1
	v_cndmask_b32_e32 v3, v229, v9, vcc
	s_waitcnt lgkmcnt(2)
	v_add_f32_e32 v6, v6, v8
	v_lshlrev_b32_e32 v3, 2, v3
	ds_bpermute_b32 v8, v3, v6
	s_waitcnt lgkmcnt(1)
	v_pk_add_f32 v[0:1], v[0:1], v[4:5]
	ds_bpermute_b32 v4, v3, v0
	ds_bpermute_b32 v5, v3, v1
	v_xor_b32_e32 v3, 2, v229
	v_cmp_lt_i32_e32 vcc, v3, v2
	s_waitcnt lgkmcnt(2)
	v_add_f32_e32 v6, v6, v8
	s_waitcnt lgkmcnt(0)
	v_pk_add_f32 v[0:1], v[0:1], v[4:5]
	v_cndmask_b32_e32 v3, v229, v3, vcc
	v_lshlrev_b32_e32 v3, 2, v3
	ds_bpermute_b32 v4, v3, v0
	ds_bpermute_b32 v5, v3, v1
	ds_bpermute_b32 v3, v3, v6
	s_waitcnt lgkmcnt(1)
	v_pk_add_f32 v[0:1], v[0:1], v[4:5]
	s_waitcnt lgkmcnt(0)
	v_add_f32_e32 v4, v6, v3
	v_xor_b32_e32 v3, 1, v229
	v_cmp_lt_i32_e32 vcc, v3, v2
	s_nop 1
	v_cndmask_b32_e32 v2, v229, v3, vcc
	v_lshlrev_b32_e32 v5, 2, v2
	ds_bpermute_b32 v2, v5, v0
	ds_bpermute_b32 v3, v5, v1
	ds_bpermute_b32 v5, v5, v4
	s_and_saveexec_b64 s[12:13], s[2:3]
	s_cbranch_execz .LBB1_5
	v_lshl_add_u32 v6, v231, 1, v231
	v_ashrrev_i32_e32 v7, 31, v6
	s_waitcnt lgkmcnt(0)
	v_add_f32_e32 v4, v4, v5
	v_lshl_add_u64 v[6:7], v[6:7], 2, s[8:9]
	v_pk_add_f32 v[2:3], v[0:1], v[2:3]
	global_store_dwordx3 v[6:7], v[2:4], off
	s_branch .LBB1_5
